# retention-output stage: gate loads hoisted above the result stores into unused VGPRs with recomputed counted waits; store-drain vmcnt(0) dropped at the P3a/P3c unit starts
# speedup vs baseline: 1.0039x; 1.0039x over previous
.LBB0_269:
	s_ashr_i32 s39, s38, 31
	s_lshr_b32 s0, s39, 28
	s_add_i32 s0, s38, s0
	s_ashr_i32 s62, s0, 4
	s_lshr_b32 s1, s62, 29
	s_add_i32 s1, s62, s1
	s_and_b32 s1, s1, -8
	s_sub_i32 s51, s62, s1
	v_cvt_f32_i32_e32 v2, s51
	s_and_b32 s0, s0, -16
	s_lshr_b32 s1, s39, 25
	s_sub_i32 s0, s38, s0
	s_add_i32 s1, s38, s1
	s_ashr_i32 s34, s1, 7
	s_ashr_i32 s1, s0, 31
	v_sub_f32_e32 v2, 0xc0a00000, v2
	s_lshl_b64 s[60:61], s[0:1], 7
	v_cmp_gt_f32_e64 s[0:1], s41, v2
	s_ashr_i32 s35, s34, 31
	s_lshl_b64 s[34:35], s[34:35], 11
	v_cndmask_b32_e64 v3, 0, v160, s[0:1]
	v_add_f32_e32 v2, v2, v3
	s_add_u32 s34, s34, s60
	v_exp_f32_e32 v2, v2
	s_addc_u32 s35, s35, s61
	s_and_b64 s[0:1], s[0:1], exec
	s_cselect_b32 s0, 0xffffffc0, 0
	v_ldexp_f32 v154, v2, s0
	v_sub_f32_e32 v4, 1.0, v154
	v_add_f32_e32 v2, -1.0, v4
	v_sub_f32_e32 v3, v2, v4
	v_add_f32_e32 v3, 1.0, v3
	v_sub_f32_e64 v2, -v154, v2
	v_add_f32_e32 v5, v2, v3
	v_frexp_mant_f32_e32 v6, v4
	v_cvt_f64_f32_e32 v[2:3], v4
	v_frexp_exp_i32_f64_e32 v2, v[2:3]
	v_cmp_gt_f32_e64 s[0:1], s42, v6
	v_mov_b64_e32 v[26:27], s[8:9]
	v_mov_b32_e32 v143, v107
	v_subbrev_co_u32_e64 v2, s[0:1], 0, v2, s[0:1]
	v_sub_u32_e32 v3, 0, v2
	v_ldexp_f32 v4, v4, v3
	v_ldexp_f32 v3, v5, v3
	v_add_f32_e32 v5, -1.0, v4
	v_add_f32_e32 v8, 1.0, v4
	v_add_f32_e32 v6, 1.0, v5
	v_add_f32_e32 v9, -1.0, v8
	v_sub_f32_e32 v6, v4, v6
	v_sub_f32_e32 v4, v4, v9
	v_add_f32_e32 v6, v3, v6
	v_add_f32_e32 v3, v3, v4
	v_add_f32_e32 v4, v8, v3
	v_rcp_f32_e32 v9, v4
	v_add_f32_e32 v7, v5, v6
	v_sub_f32_e32 v5, v7, v5
	v_sub_f32_e32 v5, v6, v5
	v_sub_f32_e32 v6, v4, v8
	v_sub_f32_e32 v3, v3, v6
	v_mul_f32_e32 v6, v7, v9
	v_mul_f32_e32 v8, v4, v6
	v_fma_f32 v10, v6, v4, -v8
	v_fmac_f32_e32 v10, v6, v3
	v_add_f32_e32 v11, v8, v10
	v_sub_f32_e32 v12, v7, v11
	v_sub_f32_e32 v7, v7, v12
	v_sub_f32_e32 v8, v11, v8
	v_sub_f32_e32 v7, v7, v11
	v_add_f32_e32 v5, v5, v7
	v_sub_f32_e32 v7, v8, v10
	v_add_f32_e32 v5, v7, v5
	v_add_f32_e32 v7, v12, v5
	v_mul_f32_e32 v8, v9, v7
	v_mul_f32_e32 v10, v4, v8
	v_fma_f32 v4, v8, v4, -v10
	v_fmac_f32_e32 v4, v8, v3
	v_sub_f32_e32 v3, v12, v7
	v_add_f32_e32 v3, v5, v3
	v_add_f32_e32 v5, v10, v4
	v_sub_f32_e32 v11, v7, v5
	v_sub_f32_e32 v7, v7, v11
	v_sub_f32_e32 v10, v5, v10
	v_sub_f32_e32 v5, v7, v5
	v_add_f32_e32 v3, v3, v5
	v_sub_f32_e32 v4, v10, v4
	v_cvt_f32_i32_e32 v2, v2
	v_add_f32_e32 v3, v4, v3
	v_add_f32_e32 v4, v6, v8
	v_add_f32_e32 v3, v11, v3
	v_sub_f32_e32 v5, v4, v6
	v_mul_f32_e32 v3, v9, v3
	v_sub_f32_e32 v5, v8, v5
	v_add_f32_e32 v3, v5, v3
	v_mul_f32_e32 v8, 0x3f317218, v2
	v_add_f32_e32 v5, v4, v3
	v_fma_f32 v9, v2, s43, -v8
	v_mul_f32_e32 v6, v5, v5
	v_fmac_f32_e32 v9, 0xb102e308, v2
	v_sub_f32_e32 v2, v5, v4
	v_fmamk_f32 v7, v6, 0x3e9b6dac, v123
	v_sub_f32_e32 v2, v3, v2
	v_add_f32_e32 v3, v8, v9
	v_fmaak_f32 v7, v6, v7, 0x3f2aaada
	v_sub_f32_e32 v4, v3, v8
	v_ldexp_f32 v8, v5, 1
	v_mul_f32_e32 v5, v5, v6
	v_mul_f32_e32 v5, v5, v7
	v_add_f32_e32 v6, v8, v5
	v_sub_f32_e32 v7, v6, v8
	v_ldexp_f32 v2, v2, 1
	v_sub_f32_e32 v5, v5, v7
	v_add_f32_e32 v2, v2, v5
	v_add_f32_e32 v5, v6, v2
	v_sub_f32_e32 v6, v5, v6
	v_sub_f32_e32 v2, v2, v6
	v_add_f32_e32 v6, v3, v5
	v_sub_f32_e32 v7, v6, v3
	v_sub_f32_e32 v8, v6, v7
	v_sub_f32_e32 v4, v9, v4
	v_sub_f32_e32 v3, v3, v8
	v_sub_f32_e32 v5, v5, v7
	v_add_f32_e32 v3, v5, v3
	v_add_f32_e32 v5, v4, v2
	v_sub_f32_e32 v7, v5, v4
	v_sub_f32_e32 v8, v5, v7
	v_add_f32_e32 v3, v5, v3
	v_sub_f32_e32 v4, v4, v8
	v_sub_f32_e32 v2, v2, v7
	v_add_f32_e32 v8, v6, v3
	v_add_f32_e32 v2, v2, v4
	v_sub_f32_e32 v4, v8, v6
	v_sub_f32_e32 v3, v3, v4
	v_add_f32_e32 v9, v2, v3
	s_lshl_b32 s0, s51, 7
	v_or_b32_e32 v2, s34, v110
	s_ashr_i32 s1, s0, 31
	v_mad_u64_u32 v[2:3], s[60:61], v2, s45, v[26:27]
	v_mad_i32_i24 v3, s35, v161, v3
	s_lshl_b64 s[60:61], s[0:1], 1
	v_lshl_add_u64 v[2:3], v[2:3], 0, s[60:61]
	v_lshl_add_u64 v[152:153], v[2:3], 0, s[14:15]
	s_lshl_b32 s0, s62, 11
	v_lshl_add_u64 v[4:5], v[152:153], 0, v[142:143]
	s_sub_i32 s62, s13, s0
	s_barrier
	global_load_dwordx4 v[164:167], v[4:5], off
	global_load_dwordx4 v[168:171], v[4:5], off offset:128
	v_add_u32_e32 v4, s62, v110
	v_ashrrev_i32_e32 v5, 31, v4
	v_lshlrev_b64 v[4:5], 8, v[4:5]
	v_lshl_add_u64 v[4:5], v[108:109], 0, v[4:5]
	v_lshl_add_u64 v[6:7], v[4:5], 0, s[18:19]
	global_load_dwordx4 v[58:61], v[4:5], off offset:16
	global_load_dwordx4 v[66:69], v[4:5], off
	v_add_co_u32_e64 v4, s[0:1], s46, v4
	v_lshl_add_u64 v[148:149], v[2:3], 0, s[22:23]
	s_nop 0
	v_addc_co_u32_e64 v5, s[0:1], 0, v5, s[0:1]
	global_load_dwordx4 v[70:73], v[4:5], off
	global_load_dwordx4 v[62:65], v[6:7], off offset:16
	v_or_b32_e32 v4, s34, v112
	v_mad_u64_u32 v[4:5], s[0:1], v4, s45, v[114:115]
	v_mad_i32_i24 v5, s35, v161, v5
	v_lshl_add_u64 v[150:151], v[4:5], 0, s[60:61]
	v_lshl_add_u64 v[4:5], v[150:151], 0, v[142:143]
	global_load_dwordx4 v[94:97], v[4:5], off
	global_load_dwordx4 v[86:89], v[4:5], off offset:128
	v_add_u32_e32 v4, s62, v112
	v_ashrrev_i32_e32 v5, 31, v4
	v_lshlrev_b64 v[4:5], 8, v[4:5]
	v_lshl_add_u64 v[4:5], v[108:109], 0, v[4:5]
	v_lshl_add_u64 v[6:7], v[4:5], 0, s[18:19]
	global_load_dwordx4 v[82:85], v[4:5], off offset:16
	global_load_dwordx4 v[98:101], v[4:5], off
	v_add_co_u32_e64 v4, s[0:1], s46, v4
	v_lshl_add_u64 v[2:3], v[148:149], 0, v[142:143]
	s_nop 0
	v_addc_co_u32_e64 v5, s[0:1], 0, v5, s[0:1]
	global_load_dwordx4 v[102:105], v[4:5], off
	global_load_dwordx4 v[90:93], v[6:7], off offset:16
	global_load_dwordx4 v[78:81], v[2:3], off
	global_load_dwordx4 v[74:77], v[2:3], off offset:128
	v_or_b32_e32 v2, s34, v116
	v_mad_u64_u32 v[2:3], s[0:1], v2, s45, v[26:27]
	v_mad_i32_i24 v3, s35, v161, v3
	v_lshl_add_u64 v[2:3], v[2:3], 0, s[60:61]
	v_lshl_add_u64 v[146:147], v[2:3], 0, s[22:23]
	v_lshl_add_u64 v[2:3], v[146:147], 0, v[142:143]
	global_load_dwordx4 v[46:49], v[2:3], off
	global_load_dwordx4 v[42:45], v[2:3], off offset:128
	v_add_u32_e32 v2, s62, v116
	v_ashrrev_i32_e32 v3, 31, v2
	v_lshlrev_b64 v[2:3], 8, v[2:3]
	v_lshl_add_u64 v[2:3], v[108:109], 0, v[2:3]
	v_lshl_add_u64 v[4:5], v[2:3], 0, s[18:19]
	global_load_dwordx4 v[34:37], v[2:3], off offset:16
	global_load_dwordx4 v[50:53], v[2:3], off
	v_add_co_u32_e64 v2, s[0:1], s46, v2
	v_mov_b32_e32 v145, v107
	s_nop 0
	v_addc_co_u32_e64 v3, s[0:1], 0, v3, s[0:1]
	global_load_dwordx4 v[54:57], v[2:3], off
	global_load_dwordx4 v[38:41], v[4:5], off offset:16
	v_add_f32_e32 v2, v8, v9
	v_cmp_nlt_f32_e64 s[0:1], 1.0, v154
	v_or_b32_e32 v4, s34, v120
	v_or_b32_e32 v10, s34, v122
	v_cndmask_b32_e64 v2, v162, v2, s[0:1]
	v_cmp_neq_f32_e64 s[0:1], 1.0, v154
	v_or_b32_e32 v12, s34, v124
	v_or_b32_e32 v18, s34, v126
	v_cndmask_b32_e64 v143, v163, v2, s[0:1]
	s_lshl_b32 s0, s51, 8
	v_or_b32_e32 v2, s34, v118
	s_ashr_i32 s1, s0, 31
	v_mad_u64_u32 v[2:3], s[60:61], v2, s45, v[26:27]
	v_mad_i32_i24 v3, s35, v161, v3
	s_lshl_b64 s[60:61], s[0:1], 1
	v_lshl_add_u64 v[2:3], v[2:3], 0, s[60:61]
	v_lshl_add_u64 v[2:3], v[2:3], 0, v[144:145]
	v_add_co_u32_e64 v2, s[0:1], s3, v2
	v_or_b32_e32 v20, s34, v128
	s_nop 0
	v_addc_co_u32_e64 v3, s[0:1], 0, v3, s[0:1]
	v_mad_u64_u32 v[4:5], s[0:1], v4, s45, v[26:27]
	v_mad_i32_i24 v5, s35, v161, v5
	v_lshl_add_u64 v[4:5], v[4:5], 0, s[60:61]
	v_lshl_add_u64 v[4:5], v[4:5], 0, v[144:145]
	v_add_co_u32_e64 v6, s[0:1], s3, v4
	v_or_b32_e32 v28, s34, v130
	s_nop 0
	v_addc_co_u32_e64 v7, s[0:1], 0, v5, s[0:1]
	v_mad_u64_u32 v[10:11], s[0:1], v10, s45, v[26:27]
	v_mad_i32_i24 v11, s35, v161, v11
	v_lshl_add_u64 v[10:11], v[10:11], 0, s[60:61]
	v_lshl_add_u64 v[10:11], v[10:11], 0, v[144:145]
	v_add_co_u32_e64 v10, s[0:1], s3, v10
	v_or_b32_e32 v30, s34, v132
	s_nop 0
	v_addc_co_u32_e64 v11, s[0:1], 0, v11, s[0:1]
	v_mad_u64_u32 v[12:13], s[0:1], v12, s45, v[26:27]
	v_mad_i32_i24 v13, s35, v161, v13
	v_lshl_add_u64 v[12:13], v[12:13], 0, s[60:61]
	v_lshl_add_u64 v[12:13], v[12:13], 0, v[144:145]
	v_add_co_u32_e64 v14, s[0:1], s3, v12
	global_load_dwordx4 v[2:5], v[2:3], off offset:2048
	s_nop 0
	global_load_dwordx4 v[6:9], v[6:7], off offset:2048
	v_addc_co_u32_e64 v15, s[0:1], 0, v13, s[0:1]
	v_mad_u64_u32 v[18:19], s[0:1], v18, s45, v[26:27]
	v_mad_i32_i24 v19, s35, v161, v19
	v_lshl_add_u64 v[18:19], v[18:19], 0, s[60:61]
	v_lshl_add_u64 v[18:19], v[18:19], 0, v[144:145]
	v_add_co_u32_e64 v18, s[0:1], s3, v18
	global_load_dwordx4 v[10:13], v[10:11], off offset:2048
	s_nop 0
	global_load_dwordx4 v[14:17], v[14:15], off offset:2048
	v_addc_co_u32_e64 v19, s[0:1], 0, v19, s[0:1]
	v_mad_u64_u32 v[20:21], s[0:1], v20, s45, v[26:27]
	v_mad_i32_i24 v21, s35, v161, v21
	v_lshl_add_u64 v[20:21], v[20:21], 0, s[60:61]
	v_lshl_add_u64 v[20:21], v[20:21], 0, v[144:145]
	v_add_co_u32_e64 v22, s[0:1], s3, v20
	v_lshl_add_u64 v[172:173], v[152:153], 0, v[106:107]
	s_nop 0
	v_addc_co_u32_e64 v23, s[0:1], 0, v21, s[0:1]
	v_mad_u64_u32 v[28:29], s[0:1], v28, s45, v[26:27]
	v_mad_i32_i24 v29, s35, v161, v29
	v_lshl_add_u64 v[28:29], v[28:29], 0, s[60:61]
	v_lshl_add_u64 v[28:29], v[28:29], 0, v[144:145]
	v_add_co_u32_e64 v28, s[0:1], s3, v28
	global_load_dwordx4 v[18:21], v[18:19], off offset:2048
	s_nop 0
	global_load_dwordx4 v[22:25], v[22:23], off offset:2048
	v_addc_co_u32_e64 v29, s[0:1], 0, v29, s[0:1]
	v_mad_u64_u32 v[26:27], s[0:1], v30, s45, v[26:27]
	v_mad_i32_i24 v27, s35, v161, v27
	v_lshl_add_u64 v[26:27], v[26:27], 0, s[60:61]
	v_lshl_add_u64 v[26:27], v[26:27], 0, v[144:145]
	v_add_co_u32_e64 v30, s[0:1], s3, v26
	s_waitcnt vmcnt(24)
	v_lshlrev_b32_e32 v177, 16, v169
	v_addc_co_u32_e64 v31, s[0:1], 0, v27, s[0:1]
	global_load_dwordx4 v[26:29], v[28:29], off offset:2048
	s_nop 0
	global_load_dwordx4 v[30:33], v[30:31], off offset:2048
	v_cmp_gt_f32_e64 s[0:1], s44, v154
	v_lshlrev_b32_e32 v176, 16, v168
	s_waitcnt vmcnt(23)
	v_mov_b32_e32 v152, v70
	v_mov_b32_e32 v153, v72
	v_cndmask_b32_e64 v143, v143, -v154, s[0:1]
	v_lshlrev_b32_e32 v175, 16, v165
	v_lshlrev_b32_e32 v174, 16, v164
	v_and_b32_e32 v165, 0xffff0000, v165
	v_and_b32_e32 v164, 0xffff0000, v164
	v_and_b32_e32 v169, 0xffff0000, v169
	v_and_b32_e32 v168, 0xffff0000, v168
	v_mov_b32_e32 v154, v66
	v_mov_b32_e32 v155, v68
	v_mov_b32_e32 v72, v71
	v_mov_b32_e32 v68, v67
	v_pk_mul_f32 v[66:67], v[152:153], v[176:177]
	v_pk_mul_f32 v[178:179], v[152:153], v[174:175]
	v_pk_mul_f32 v[70:71], v[72:73], v[164:165]
	v_pk_fma_f32 v[174:175], v[154:155], v[174:175], v[66:67] neg_lo:[0,0,1] neg_hi:[0,0,1]
	v_pk_mul_f32 v[66:67], v[72:73], v[168:169]
	v_pk_fma_f32 v[180:181], v[68:69], v[168:169], v[70:71]
	v_pk_fma_f32 v[164:165], v[68:69], v[164:165], v[66:67] neg_lo:[0,0,1] neg_hi:[0,0,1]
	v_lshlrev_b32_e32 v169, 16, v167
	v_lshlrev_b32_e32 v168, 16, v166
	v_and_b32_e32 v167, 0xffff0000, v167
	v_and_b32_e32 v166, 0xffff0000, v166
	s_waitcnt vmcnt(22)
	v_mov_b32_e32 v67, v64
	v_mov_b32_e32 v64, v63
	v_pk_fma_f32 v[178:179], v[154:155], v[176:177], v[178:179]
	v_lshlrev_b32_e32 v177, 16, v171
	v_lshlrev_b32_e32 v176, 16, v170
	v_and_b32_e32 v171, 0xffff0000, v171
	v_and_b32_e32 v170, 0xffff0000, v170
	v_mov_b32_e32 v66, v62
	v_mov_b32_e32 v71, v60
	v_pk_mul_f32 v[62:63], v[64:65], v[166:167]
	v_mov_b32_e32 v60, v59
	v_mov_b32_e32 v70, v58
	v_pk_fma_f32 v[58:59], v[60:61], v[170:171], v[62:63]
	v_pk_mul_f32 v[62:63], v[66:67], v[176:177]
	v_pk_mul_f32 v[182:183], v[66:67], v[168:169]
	v_pk_fma_f32 v[62:63], v[70:71], v[168:169], v[62:63] neg_lo:[0,0,1] neg_hi:[0,0,1]
	v_pk_mul_f32 v[168:169], v[64:65], v[170:171]
	v_bfe_u32 v170, v164, 16, 1
	v_pk_fma_f32 v[166:167], v[60:61], v[166:167], v[168:169] neg_lo:[0,0,1] neg_hi:[0,0,1]
	v_bfe_u32 v169, v165, 16, 1
	v_bfe_u32 v145, v167, 16, 1
	v_add3_u32 v164, v164, v170, s50
	v_add3_u32 v165, v165, v169, s50
	v_add3_u32 v145, v167, v145, s50
	v_bfe_u32 v167, v174, 16, 1
	v_bfe_u32 v169, v62, 16, 1
	v_bfe_u32 v170, v63, 16, 1
	v_bfe_u32 v168, v166, 16, 1
	v_add3_u32 v63, v63, v170, s50
	v_add3_u32 v62, v62, v169, s50
	v_add3_u32 v167, v174, v167, s50
	v_pk_fma_f32 v[182:183], v[70:71], v[176:177], v[182:183]
	v_add3_u32 v166, v166, v168, s50
	v_bfe_u32 v168, v175, 16, 1
	v_lshrrev_b32_e32 v169, 16, v167
	v_lshrrev_b32_e32 v62, 16, v62
	v_lshrrev_b32_e32 v63, 16, v63
	v_add3_u32 v168, v175, v168, s50
	v_and_or_b32 v167, v145, s47, v63
	v_and_or_b32 v166, v166, s47, v62
	v_and_or_b32 v164, v164, s47, v169
	v_bfe_u32 v62, v59, 16, 1
	v_bfe_u32 v63, v58, 16, 1
	v_bfe_u32 v169, v182, 16, 1
	v_bfe_u32 v170, v183, 16, 1
	v_lshrrev_b32_e32 v168, 16, v168
	v_add3_u32 v58, v58, v63, s50
	v_add3_u32 v59, v59, v62, s50
	v_bfe_u32 v62, v178, 16, 1
	v_bfe_u32 v63, v179, 16, 1
	v_add3_u32 v170, v183, v170, s50
	v_add3_u32 v169, v182, v169, s50
	v_and_or_b32 v165, v165, s47, v168
	v_bfe_u32 v145, v181, 16, 1
	v_bfe_u32 v168, v180, 16, 1
	v_add3_u32 v63, v179, v63, s50
	v_add3_u32 v62, v178, v62, s50
	v_lshrrev_b32_e32 v169, 16, v169
	v_lshrrev_b32_e32 v170, 16, v170
	v_add3_u32 v168, v180, v168, s50
	v_add3_u32 v145, v181, v145, s50
	v_lshrrev_b32_e32 v62, 16, v62
	v_lshrrev_b32_e32 v63, 16, v63
	v_and_or_b32 v171, v59, s47, v170
	v_and_or_b32 v170, v58, s47, v169
	v_and_or_b32 v169, v145, s47, v63
	v_and_or_b32 v168, v168, s47, v62
	global_store_dwordx4 v[172:173], v[164:167], off
	global_store_dwordx4 v[172:173], v[168:171], off offset:128
	s_waitcnt vmcnt(22)
	v_lshlrev_b32_e32 v63, 16, v87
	v_lshlrev_b32_e32 v62, 16, v86
	s_waitcnt vmcnt(19)
	v_mov_b32_e32 v170, v102
	v_mov_b32_e32 v171, v104
	v_lshlrev_b32_e32 v59, 16, v95
	v_lshlrev_b32_e32 v58, 16, v94
	v_and_b32_e32 v167, 0xffff0000, v87
	v_and_b32_e32 v166, 0xffff0000, v86
	v_mov_b32_e32 v168, v98
	v_mov_b32_e32 v169, v100
	v_pk_mul_f32 v[86:87], v[170:171], v[62:63]
	v_and_b32_e32 v165, 0xffff0000, v95
	v_and_b32_e32 v164, 0xffff0000, v94
	v_pk_fma_f32 v[86:87], v[168:169], v[58:59], v[86:87] neg_lo:[0,0,1] neg_hi:[0,0,1]
	v_mov_b32_e32 v104, v103
	v_pk_mul_f32 v[58:59], v[170:171], v[58:59]
	v_mov_b32_e32 v100, v99
	v_pk_mul_f32 v[94:95], v[104:105], v[166:167]
	v_pk_fma_f32 v[58:59], v[168:169], v[62:63], v[58:59]
	v_pk_mul_f32 v[62:63], v[104:105], v[164:165]
	v_pk_fma_f32 v[94:95], v[100:101], v[164:165], v[94:95] neg_lo:[0,0,1] neg_hi:[0,0,1]
	v_pk_fma_f32 v[62:63], v[100:101], v[166:167], v[62:63]
	v_lshlrev_b32_e32 v101, 16, v89
	v_lshlrev_b32_e32 v100, 16, v88
	v_and_b32_e32 v103, 0xffff0000, v89
	v_and_b32_e32 v102, 0xffff0000, v88
	s_waitcnt vmcnt(18)
	v_mov_b32_e32 v164, v90
	v_mov_b32_e32 v165, v92
	v_mov_b32_e32 v92, v91
	v_lshlrev_b32_e32 v99, 16, v97
	v_lshlrev_b32_e32 v98, 16, v96
	v_and_b32_e32 v97, 0xffff0000, v97
	v_and_b32_e32 v96, 0xffff0000, v96
	v_mov_b32_e32 v104, v82
	v_mov_b32_e32 v105, v84
	v_pk_mul_f32 v[88:89], v[164:165], v[100:101]
	v_mov_b32_e32 v84, v83
	v_pk_mul_f32 v[82:83], v[92:93], v[102:103]
	v_pk_mul_f32 v[94:95], v[134:135], v[94:95]
	v_pk_fma_f32 v[88:89], v[104:105], v[98:99], v[88:89] neg_lo:[0,0,1] neg_hi:[0,0,1]
	v_pk_fma_f32 v[82:83], v[84:85], v[96:97], v[82:83] neg_lo:[0,0,1] neg_hi:[0,0,1]
	v_pk_mul_f32 v[86:87], v[134:135], v[86:87]
	v_pk_mul_f32 v[88:89], v[134:135], v[88:89]
	v_pk_mul_f32 v[90:91], v[134:135], v[82:83]
	v_pk_mul_f32 v[82:83], v[164:165], v[98:99]
	v_pk_mul_f32 v[92:93], v[92:93], v[96:97]
	v_bfe_u32 v98, v95, 16, 1
	v_bfe_u32 v99, v94, 16, 1
	v_pk_fma_f32 v[82:83], v[104:105], v[100:101], v[82:83]
	v_pk_fma_f32 v[84:85], v[84:85], v[102:103], v[92:93]
	v_add3_u32 v100, v94, v99, s50
	v_add3_u32 v101, v95, v98, s50
	v_bfe_u32 v98, v86, 16, 1
	v_bfe_u32 v99, v87, 16, 1
	v_bfe_u32 v102, v88, 16, 1
	v_bfe_u32 v103, v89, 16, 1
	v_pk_mul_f32 v[62:63], v[134:135], v[62:63]
	v_bfe_u32 v96, v91, 16, 1
	v_bfe_u32 v97, v90, 16, 1
	v_add3_u32 v103, v89, v103, s50
	v_add3_u32 v102, v88, v102, s50
	v_add3_u32 v99, v87, v99, s50
	v_add3_u32 v98, v86, v98, s50
	v_pk_mul_f32 v[58:59], v[134:135], v[58:59]
	v_pk_mul_f32 v[82:83], v[134:135], v[82:83]
	v_add3_u32 v97, v90, v97, s50
	v_add3_u32 v96, v91, v96, s50
	v_lshrrev_b32_e32 v104, 16, v98
	v_lshrrev_b32_e32 v105, 16, v99
	v_lshrrev_b32_e32 v98, 16, v102
	v_lshrrev_b32_e32 v99, 16, v103
	v_bfe_u32 v102, v63, 16, 1
	v_bfe_u32 v103, v62, 16, 1
	v_pk_mul_f32 v[84:85], v[134:135], v[84:85]
	v_lshl_add_u64 v[92:93], v[150:151], 0, v[106:107]
	v_and_or_b32 v99, v96, s47, v99
	v_and_or_b32 v98, v97, s47, v98
	v_and_or_b32 v97, v101, s47, v105
	v_and_or_b32 v96, v100, s47, v104
	v_add3_u32 v104, v62, v103, s50
	v_add3_u32 v105, v63, v102, s50
	v_bfe_u32 v102, v58, 16, 1
	v_bfe_u32 v103, v59, 16, 1
	v_bfe_u32 v145, v82, 16, 1
	v_bfe_u32 v150, v83, 16, 1
	v_bfe_u32 v100, v85, 16, 1
	v_bfe_u32 v101, v84, 16, 1
	v_add3_u32 v150, v83, v150, s50
	v_add3_u32 v145, v82, v145, s50
	v_add3_u32 v103, v59, v103, s50
	v_add3_u32 v102, v58, v102, s50
	v_add3_u32 v101, v84, v101, s50
	v_add3_u32 v100, v85, v100, s50
	v_lshrrev_b32_e32 v151, 16, v102
	v_lshrrev_b32_e32 v164, 16, v103
	v_lshrrev_b32_e32 v102, 16, v145
	v_lshrrev_b32_e32 v103, 16, v150
	v_and_or_b32 v103, v100, s47, v103
	v_and_or_b32 v102, v101, s47, v102
	v_and_or_b32 v101, v105, s47, v164
	v_and_or_b32 v100, v104, s47, v151
	global_store_dwordx4 v[92:93], v[96:99], off
	global_store_dwordx4 v[92:93], v[100:103], off offset:128
	s_and_saveexec_b64 s[0:1], vcc
	s_cbranch_execz .LBB0_268
	v_mul_f32_e32 v92, v143, v111
	v_mul_f32_e32 v92, 0x3fb8aa3b, v92
	v_exp_f32_e32 v92, v92
	s_nop 0
	v_pk_mul_f32 v[94:95], v[92:93], v[94:95] op_sel_hi:[0,1]
	v_pk_mul_f32 v[88:89], v[92:93], v[88:89] op_sel_hi:[0,1]
	v_pk_mul_f32 v[90:91], v[92:93], v[90:91] op_sel_hi:[0,1]
	v_bfe_u32 v97, v95, 16, 1
	v_bfe_u32 v98, v94, 16, 1
	v_pk_mul_f32 v[86:87], v[92:93], v[86:87] op_sel_hi:[0,1]
	v_bfe_u32 v93, v91, 16, 1
	v_add3_u32 v94, v94, v98, s50
	v_add3_u32 v95, v95, v97, s50
	v_bfe_u32 v97, v88, 16, 1
	v_bfe_u32 v98, v89, 16, 1
	v_bfe_u32 v96, v90, 16, 1
	v_add3_u32 v91, v91, v93, s50
	v_bfe_u32 v93, v86, 16, 1
	v_add3_u32 v89, v89, v98, s50
	v_add3_u32 v88, v88, v97, s50
	v_add3_u32 v90, v90, v96, s50
	v_lshrrev_b32_e32 v88, 16, v88
	v_lshrrev_b32_e32 v89, 16, v89
	v_pk_mul_f32 v[62:63], v[92:93], v[62:63] op_sel_hi:[0,1]
	v_pk_mul_f32 v[84:85], v[92:93], v[84:85] op_sel_hi:[0,1]
	v_bfe_u32 v96, v87, 16, 1
	v_add3_u32 v86, v86, v93, s50
	v_and_or_b32 v89, v91, s47, v89
	v_and_or_b32 v88, v90, s47, v88
	v_pk_mul_f32 v[58:59], v[92:93], v[58:59] op_sel_hi:[0,1]
	v_pk_mul_f32 v[82:83], v[92:93], v[82:83] op_sel_hi:[0,1]
	v_bfe_u32 v90, v85, 16, 1
	v_bfe_u32 v91, v84, 16, 1
	v_bfe_u32 v92, v63, 16, 1
	v_bfe_u32 v93, v62, 16, 1
	v_add3_u32 v87, v87, v96, s50
	v_add3_u32 v62, v62, v93, s50
	v_add3_u32 v63, v63, v92, s50
	v_add3_u32 v84, v84, v91, s50
	v_add3_u32 v85, v85, v90, s50
	v_bfe_u32 v90, v58, 16, 1
	v_bfe_u32 v91, v59, 16, 1
	v_bfe_u32 v92, v82, 16, 1
	v_bfe_u32 v93, v83, 16, 1
	v_lshrrev_b32_e32 v86, 16, v86
	v_lshrrev_b32_e32 v87, 16, v87
	v_add3_u32 v83, v83, v93, s50
	v_add3_u32 v82, v82, v92, s50
	v_add3_u32 v59, v59, v91, s50
	v_add3_u32 v58, v58, v90, s50
	v_and_or_b32 v87, v95, s47, v87
	v_and_or_b32 v86, v94, s47, v86
	v_lshrrev_b32_e32 v58, 16, v58
	v_lshrrev_b32_e32 v59, 16, v59
	v_lshrrev_b32_e32 v82, 16, v82
	v_lshrrev_b32_e32 v83, 16, v83
	v_and_or_b32 v85, v85, s47, v83
	v_and_or_b32 v84, v84, s47, v82
	v_and_or_b32 v83, v63, s47, v59
	v_and_or_b32 v82, v62, s47, v58
	ds_write_b128 v125, v[86:89]
	ds_write_b128 v125, v[82:85] offset:128
	s_branch .LBB0_268

.LBB0_389:
	s_ashr_i32 s41, s40, 31
	s_lshr_b32 s0, s41, 28
	s_add_i32 s0, s40, s0
	s_ashr_i32 s1, s0, 4
	s_and_b32 s0, s0, -16
	s_sub_i32 s42, s40, s0
	s_lshr_b32 s0, s1, 29
	s_add_i32 s0, s1, s0
	s_and_b32 s0, s0, -8
	s_sub_i32 s34, s1, s0
	s_lshr_b32 s0, s41, 25
	s_add_i32 s0, s40, s0
	v_cvt_f32_i32_e32 v2, s34
	s_ashr_i32 s0, s0, 7
	s_ashr_i32 s1, s0, 31
	s_ashr_i32 s43, s42, 31
	s_lshl_b64 s[0:1], s[0:1], 11
	s_lshl_b64 s[4:5], s[42:43], 7
	s_add_u32 s4, s0, s4
	v_sub_f32_e32 v14, 0xc0a00000, v2
	s_addc_u32 s5, s1, s5
	v_cmp_gt_f32_e32 vcc, s46, v14
	s_and_b64 s[0:1], vcc, exec
	s_cselect_b32 s35, 0xffffffc0, 0
	s_lshl_b32 s6, s34, 7
	v_or_b32_e32 v2, s4, v116
	v_mov_b64_e32 v[10:11], s[14:15]
	s_ashr_i32 s7, s6, 31
	v_mad_u64_u32 v[2:3], s[0:1], v2, s49, v[10:11]
	v_mad_i32_i24 v3, s5, v169, v3
	s_lshl_b64 s[0:1], s[6:7], 1
	v_or_b32_e32 v4, s4, v118
	v_lshl_add_u64 v[2:3], v[2:3], 0, s[0:1]
	v_mad_u64_u32 v[4:5], s[8:9], v4, s49, v[10:11]
	v_lshl_add_u64 v[2:3], v[2:3], 0, v[114:115]
	v_mad_i32_i24 v5, s5, v169, v5
	v_or_b32_e32 v12, s4, v120
	v_cndmask_b32_e32 v15, 0, v168, vcc
	v_add_co_u32_e32 v2, vcc, s50, v2
	v_lshl_add_u64 v[4:5], v[4:5], 0, s[0:1]
	v_mad_u64_u32 v[12:13], s[8:9], v12, s49, v[10:11]
	v_addc_co_u32_e32 v3, vcc, 0, v3, vcc
	v_lshl_add_u64 v[4:5], v[4:5], 0, v[114:115]
	v_mad_i32_i24 v13, s5, v169, v13
	v_or_b32_e32 v16, s4, v122
	v_add_co_u32_e32 v6, vcc, s50, v4
	v_lshl_add_u64 v[12:13], v[12:13], 0, s[0:1]
	v_mad_u64_u32 v[10:11], s[8:9], v16, s49, v[10:11]
	v_addc_co_u32_e32 v7, vcc, 0, v5, vcc
	v_lshl_add_u64 v[12:13], v[12:13], 0, v[114:115]
	v_mad_i32_i24 v11, s5, v169, v11
	v_add_co_u32_e32 v12, vcc, s50, v12
	v_lshl_add_u64 v[10:11], v[10:11], 0, s[0:1]
	s_nop 0
	v_addc_co_u32_e32 v13, vcc, 0, v13, vcc
	v_lshl_add_u64 v[10:11], v[10:11], 0, v[114:115]
	v_add_co_u32_e32 v10, vcc, 0x2000, v10
	s_barrier
	global_load_dwordx4 v[2:5], v[2:3], off
	s_nop 0
	global_load_dwordx4 v[6:9], v[6:7], off
	v_addc_co_u32_e32 v11, vcc, 0, v11, vcc
	global_load_dwordx4 v[22:25], v[12:13], off
	global_load_dwordx4 v[18:21], v[10:11], off
	v_add_f32_e32 v10, v14, v15
	v_exp_f32_e32 v10, v10
	s_cmp_gt_i32 s42, 0
	s_cselect_b64 s[8:9], -1, 0
	s_cmp_lt_i32 s42, 1
	v_ldexp_f32 v51, v10, s35
	v_sub_f32_e32 v50, 1.0, v51
	v_frexp_mant_f32_e32 v10, v50
	s_cselect_b64 s[44:45], -1, 0
	v_cmp_gt_f32_e64 s[0:1], s47, v10
	s_and_b64 vcc, exec, s[44:45]
	s_cbranch_vccnz .LBB0_391
	s_lshl_b64 s[42:43], s[40:41], 16
	v_lshl_add_u64 v[42:43], v[126:127], 0, s[42:43]
	v_add_co_u32_e32 v14, vcc, 0x2000, v42
	s_nop 1
	v_addc_co_u32_e32 v15, vcc, 0, v43, vcc
	v_add_co_u32_e32 v26, vcc, 0x4000, v42
	global_load_dwordx4 v[10:13], v[42:43], off
	s_nop 0
	global_load_dwordx4 v[14:17], v[14:15], off
	v_addc_co_u32_e32 v27, vcc, 0, v43, vcc
	v_add_co_u32_e32 v30, vcc, 0x6000, v42
	s_nop 1
	v_addc_co_u32_e32 v31, vcc, 0, v43, vcc
	v_add_co_u32_e32 v34, vcc, 0x8000, v42
	global_load_dwordx4 v[26:29], v[26:27], off
	s_nop 0
	global_load_dwordx4 v[30:33], v[30:31], off
	v_addc_co_u32_e32 v35, vcc, 0, v43, vcc
	v_add_co_u32_e32 v38, vcc, 0xa000, v42
	s_nop 1
	v_addc_co_u32_e32 v39, vcc, 0, v43, vcc
	v_add_co_u32_e32 v44, vcc, 0xc000, v42
	global_load_dwordx4 v[34:37], v[34:35], off
	s_nop 0
	global_load_dwordx4 v[38:41], v[38:39], off
	v_addc_co_u32_e32 v45, vcc, 0, v43, vcc
	v_add_co_u32_e32 v46, vcc, 0xe000, v42
	s_nop 1
	v_addc_co_u32_e32 v47, vcc, 0, v43, vcc
	global_load_dwordx4 v[42:45], v[44:45], off
	s_nop 0
	global_load_dwordx4 v[46:49], v[46:47], off

.LBB0_399:
	ds_read_b128 v[86:89], v83
	ds_read_b128 v[90:93], v83 offset:64
	ds_read_b128 v[94:97], v83 offset:4608
	ds_read_b128 v[98:101], v83 offset:128
	ds_read_b128 v[102:105], v83 offset:4672
	v_add_u32_e32 v85, s0, v137
	s_waitcnt lgkmcnt(2)
	v_mfma_f32_16x16x32_bf16 v[94:97], v[94:97], v[74:77], 0
	ds_read_b128 v[106:109], v83 offset:192
	ds_read_b128 v[110:113], v83 offset:4736
	ds_read_b128 v[178:181], v83 offset:4800
	v_cmp_ge_u32_e32 vcc, v146, v82
	v_mfma_f32_16x16x32_bf16 v[86:89], v[86:89], v[74:77], 0
	v_mfma_f32_16x16x32_bf16 v[86:89], v[90:93], v[66:69], v[86:89]
	v_cvt_f32_i32_e32 v90, v85
	v_add_u32_e32 v91, -1, v85
	v_cvt_f32_i32_e32 v91, v91
	s_waitcnt lgkmcnt(4)
	v_mfma_f32_16x16x32_bf16 v[86:89], v[98:101], v[70:73], v[86:89]
	v_mul_f32_e32 v90, v149, v90
	v_mul_f32_e32 v90, 0x3fb8aa3b, v90
	v_mul_f32_e32 v91, v149, v91
	v_exp_f32_e32 v98, v90
	v_mul_f32_e32 v99, 0x3fb8aa3b, v91
	s_waitcnt lgkmcnt(3)
	v_mfma_f32_16x16x32_bf16 v[90:93], v[102:105], v[66:69], v[94:97]
	v_exp_f32_e32 v99, v99
	s_nop 1
	v_add_u32_e32 v94, -2, v85
	v_cvt_f32_i32_e32 v94, v94
	v_add_u32_e32 v97, -3, v85
	s_waitcnt lgkmcnt(2)
	v_mfma_f32_16x16x32_bf16 v[86:89], v[106:109], v[78:81], v[86:89]
	v_add_u32_e32 v95, 2, v82
	v_mul_f32_e32 v94, v149, v94
	v_mul_f32_e32 v94, 0x3fb8aa3b, v94
	v_exp_f32_e32 v96, v94
	v_cndmask_b32_e32 v94, 0, v98, vcc
	v_cvt_f32_i32_e32 v98, v97
	v_cmp_ge_u32_e32 vcc, v1, v95
	s_nop 0
	v_mov_b32_e32 v97, v88
	v_add_u32_e32 v88, 3, v82
	v_cndmask_b32_e32 v95, 0, v96, vcc
	v_mov_b32_e32 v96, v86
	v_mul_f32_e32 v86, v149, v98
	v_mul_f32_e32 v86, 0x3fb8aa3b, v86
	v_exp_f32_e32 v86, v86
	v_cmp_le_u32_e32 vcc, v88, v124
	v_pk_mul_f32 v[94:95], v[94:95], v[96:97]
	v_mov_b32_e32 v88, v87
	v_cndmask_b32_e32 v97, 0, v86, vcc
	v_cmp_gt_u32_e32 vcc, v146, v82
	v_add_u32_e32 v86, -16, v85
	v_cvt_f32_i32_e32 v98, v86
	v_cndmask_b32_e32 v96, 0, v99, vcc
	v_pk_mul_f32 v[86:87], v[96:97], v[88:89]
	v_subrev_u32_e32 v96, 18, v85
	v_cvt_f32_i32_e32 v96, v96
	v_subrev_u32_e32 v89, 17, v85
	v_subrev_u32_e32 v85, 19, v85
	s_waitcnt lgkmcnt(1)
	v_mfma_f32_16x16x32_bf16 v[90:93], v[110:113], v[70:73], v[90:93]
	v_cvt_f32_i32_e32 v89, v89
	v_cvt_f32_i32_e32 v85, v85
	v_mul_f32_e32 v96, v149, v96
	v_mul_f32_e32 v88, v149, v98
	v_mul_f32_e32 v96, 0x3fb8aa3b, v96
	s_waitcnt lgkmcnt(0)
	v_mfma_f32_16x16x32_bf16 v[90:93], v[178:181], v[78:81], v[90:93]
	v_mul_f32_e32 v88, 0x3fb8aa3b, v88
	v_mul_f32_e32 v89, v149, v89
	v_exp_f32_e32 v96, v96
	v_mul_f32_e32 v85, v149, v85
	v_exp_f32_e32 v88, v88
	v_mul_f32_e32 v89, 0x3fb8aa3b, v89
	v_mul_f32_e32 v85, 0x3fb8aa3b, v85
	v_exp_f32_e32 v98, v89
	v_add_u32_e32 v89, 18, v82
	v_exp_f32_e32 v85, v85
	v_add_u32_e32 v99, 16, v82
	v_cmp_ge_u32_e32 vcc, v1, v89
	v_mov_b32_e32 v97, v92
	v_mov_b32_e32 v92, v91
	v_cndmask_b32_e32 v89, 0, v96, vcc
	v_cmp_ge_u32_e32 vcc, v146, v99
	v_mov_b32_e32 v96, v90
	v_add_u32_e32 v90, 19, v82
	v_cndmask_b32_e32 v88, 0, v88, vcc
	v_cmp_le_u32_e32 vcc, v90, v124
	v_pk_mul_f32 v[88:89], v[88:89], v[96:97]
	s_nop 0
	v_cndmask_b32_e32 v97, 0, v85, vcc
	v_cmp_gt_u32_e32 vcc, v146, v99
	s_nop 1
	v_cndmask_b32_e32 v96, 0, v98, vcc
	v_pk_mul_f32 v[90:91], v[96:97], v[92:93]
	v_bfe_u32 v93, v87, 16, 1
	v_bfe_u32 v85, v91, 16, 1
	v_bfe_u32 v92, v90, 16, 1
	v_add3_u32 v87, v87, v93, s63
	v_add3_u32 v85, v91, v85, s63
	v_bfe_u32 v91, v94, 16, 1
	v_bfe_u32 v93, v88, 16, 1
	v_bfe_u32 v96, v86, 16, 1
	v_add3_u32 v90, v90, v92, s63
	v_bfe_u32 v92, v95, 16, 1
	v_add3_u32 v88, v88, v93, s63
	v_add3_u32 v91, v94, v91, s63
	v_add3_u32 v86, v86, v96, s63
	v_add3_u32 v92, v95, v92, s63
	v_lshrrev_b32_e32 v91, 16, v91
	v_lshrrev_b32_e32 v88, 16, v88
	v_lshrrev_b32_e32 v92, 16, v92
	v_and_or_b32 v88, v90, s64, v88
	v_and_or_b32 v86, v86, s64, v91
	ds_read_b64_tr_b16 v[90:91], v84 offset:0
	v_and_or_b32 v87, v87, s64, v92
	ds_read_b64_tr_b16 v[92:93], v84 offset:8704
	v_bfe_u32 v96, v89, 16, 1
	ds_read_b64_tr_b16 v[94:95], v84 offset:32
	v_add3_u32 v89, v89, v96, s63
	ds_read_b64_tr_b16 v[96:97], v84 offset:8736
	ds_read_b64_tr_b16 v[98:99], v84 offset:64
	ds_read_b64_tr_b16 v[100:101], v84 offset:8768
	ds_read_b64_tr_b16 v[102:103], v84 offset:96
	ds_read_b64_tr_b16 v[104:105], v84 offset:8800
	ds_read_b64_tr_b16 v[106:107], v84 offset:128
	ds_read_b64_tr_b16 v[108:109], v84 offset:8832
	ds_read_b64_tr_b16 v[110:111], v84 offset:160
	ds_read_b64_tr_b16 v[112:113], v84 offset:8864
	ds_read_b64_tr_b16 v[178:179], v84 offset:192
	ds_read_b64_tr_b16 v[180:181], v84 offset:8896
	ds_read_b64_tr_b16 v[182:183], v84 offset:224
	ds_read_b64_tr_b16 v[184:185], v84 offset:8928
	s_waitcnt lgkmcnt(0)
	v_lshrrev_b32_e32 v89, 16, v89
	v_and_or_b32 v89, v85, s64, v89
	s_nop 1
	v_mfma_f32_16x16x32_bf16 v[62:65], v[90:93], v[86:89], v[62:65]
	ds_read_b64_tr_b16 v[90:91], v84 offset:256
	ds_read_b64_tr_b16 v[92:93], v84 offset:8960
	v_mfma_f32_16x16x32_bf16 v[58:61], v[94:97], v[86:89], v[58:61]
	ds_read_b64_tr_b16 v[94:95], v84 offset:288
	ds_read_b64_tr_b16 v[96:97], v84 offset:8992
	v_mfma_f32_16x16x32_bf16 v[54:57], v[98:101], v[86:89], v[54:57]
	ds_read_b64_tr_b16 v[98:99], v84 offset:320
	ds_read_b64_tr_b16 v[100:101], v84 offset:9024
	v_mfma_f32_16x16x32_bf16 v[50:53], v[102:105], v[86:89], v[50:53]
	ds_read_b64_tr_b16 v[102:103], v84 offset:352
	ds_read_b64_tr_b16 v[104:105], v84 offset:9056
	v_mfma_f32_16x16x32_bf16 v[46:49], v[106:109], v[86:89], v[46:49]
	ds_read_b64_tr_b16 v[106:107], v84 offset:384
	ds_read_b64_tr_b16 v[108:109], v84 offset:9088
	v_mfma_f32_16x16x32_bf16 v[42:45], v[110:113], v[86:89], v[42:45]
	ds_read_b64_tr_b16 v[110:111], v84 offset:416
	ds_read_b64_tr_b16 v[112:113], v84 offset:9120
	ds_read_b64_tr_b16 v[186:187], v84 offset:448
	ds_read_b64_tr_b16 v[188:189], v84 offset:9152
	v_mfma_f32_16x16x32_bf16 v[38:41], v[178:181], v[86:89], v[38:41]
	ds_read_b64_tr_b16 v[178:179], v84 offset:480
	ds_read_b64_tr_b16 v[180:181], v84 offset:9184
	s_waitcnt lgkmcnt(0)
	v_mfma_f32_16x16x32_bf16 v[34:37], v[182:185], v[86:89], v[34:37]
	v_mfma_f32_16x16x32_bf16 v[30:33], v[90:93], v[86:89], v[30:33]
	s_sub_i32 s0, s0, 32
	s_add_i32 s1, s3, s0
	v_add_u32_e32 v84, 0x4400, v84
	v_mfma_f32_16x16x32_bf16 v[26:29], v[94:97], v[86:89], v[26:29]
	v_add_u32_e32 v83, 0x2400, v83
	v_add_u32_e32 v82, 32, v82
	s_cmp_lg_u32 s1, 0
	v_mfma_f32_16x16x32_bf16 v[22:25], v[98:101], v[86:89], v[22:25]
	v_mfma_f32_16x16x32_bf16 v[18:21], v[102:105], v[86:89], v[18:21]
	v_mfma_f32_16x16x32_bf16 v[14:17], v[106:109], v[86:89], v[14:17]
	v_mfma_f32_16x16x32_bf16 v[10:13], v[110:113], v[86:89], v[10:13]
	v_mfma_f32_16x16x32_bf16 v[6:9], v[186:189], v[86:89], v[6:9]
	v_mfma_f32_16x16x32_bf16 v[2:5], v[178:181], v[86:89], v[2:5]
	s_cbranch_scc1 .LBB0_399
	v_pk_mul_f32 v[66:67], v[64:65], v[64:65]
	v_pk_mul_f32 v[68:69], v[62:63], v[62:63]
	v_mov_b32_e32 v153, v115
	v_pk_mov_b32 v[70:71], v[68:69], v[66:67] op_sel:[1,0]
	v_mov_b32_e32 v69, v67
	v_pk_add_f32 v[66:67], v[70:71], v[68:69]
	v_pk_mul_f32 v[68:69], v[60:61], v[60:61]
	v_pk_mul_f32 v[70:71], v[58:59], v[58:59]
	v_pk_add_f32 v[66:67], v[66:67], v[66:67] op_sel:[0,1] op_sel_hi:[1,0]
	v_pk_mov_b32 v[72:73], v[70:71], v[68:69] op_sel:[1,0]
	v_mov_b32_e32 v71, v69
	v_pk_add_f32 v[68:69], v[72:73], v[70:71]
	v_mul_f32_e32 v70, v50, v50
	v_mul_f32_e32 v71, v51, v51
	v_pk_add_f32 v[68:69], v[68:69], v[68:69] op_sel:[0,1] op_sel_hi:[1,0]
	v_mov_b32_e32 v67, v70
	v_mov_b32_e32 v69, v71
	v_pk_add_f32 v[66:67], v[66:67], v[68:69]
	v_mul_f32_e32 v68, v55, v55
	v_mul_f32_e32 v70, v57, v57
	v_mul_f32_e32 v72, v52, v52
	v_mul_f32_e32 v73, v53, v53
	v_pk_fma_f32 v[68:69], v[54:55], v[54:55], v[68:69] op_sel_hi:[1,1,0]
	v_pk_fma_f32 v[70:71], v[56:57], v[56:57], v[70:71] op_sel_hi:[1,1,0]
	v_mov_b32_e32 v69, v72
	v_mov_b32_e32 v71, v73
	v_pk_add_f32 v[68:69], v[68:69], v[70:71]
	v_pk_mul_f32 v[70:71], v[46:47], v[46:47]
	v_pk_add_f32 v[66:67], v[66:67], v[68:69]
	v_pk_mul_f32 v[68:69], v[48:49], v[48:49]
	v_pk_add_f32 v[66:67], v[66:67], v[66:67] op_sel:[0,1] op_sel_hi:[1,0]
	v_pk_mov_b32 v[72:73], v[70:71], v[68:69] op_sel:[1,0]
	v_mov_b32_e32 v71, v69
	v_pk_add_f32 v[68:69], v[72:73], v[70:71]
	v_mul_f32_e32 v70, v38, v38
	v_mul_f32_e32 v71, v39, v39
	v_pk_add_f32 v[68:69], v[68:69], v[68:69] op_sel:[0,1] op_sel_hi:[1,0]
	v_mov_b32_e32 v67, v70
	v_mov_b32_e32 v69, v71
	v_pk_add_f32 v[66:67], v[66:67], v[68:69]
	v_mul_f32_e32 v68, v43, v43
	v_mul_f32_e32 v70, v45, v45
	v_mul_f32_e32 v72, v40, v40
	v_mul_f32_e32 v73, v41, v41
	v_pk_fma_f32 v[68:69], v[42:43], v[42:43], v[68:69] op_sel_hi:[1,1,0]
	v_pk_fma_f32 v[70:71], v[44:45], v[44:45], v[70:71] op_sel_hi:[1,1,0]
	v_mov_b32_e32 v69, v72
	v_mov_b32_e32 v71, v73
	v_pk_add_f32 v[68:69], v[68:69], v[70:71]
	v_pk_mul_f32 v[70:71], v[34:35], v[34:35]
	v_pk_add_f32 v[66:67], v[66:67], v[68:69]
	v_pk_mul_f32 v[68:69], v[36:37], v[36:37]
	v_pk_add_f32 v[66:67], v[66:67], v[66:67] op_sel:[0,1] op_sel_hi:[1,0]
	v_pk_mov_b32 v[72:73], v[70:71], v[68:69] op_sel:[1,0]
	v_mov_b32_e32 v71, v69
	v_pk_add_f32 v[68:69], v[72:73], v[70:71]
	v_mul_f32_e32 v70, v26, v26
	v_mul_f32_e32 v71, v27, v27
	v_pk_add_f32 v[68:69], v[68:69], v[68:69] op_sel:[0,1] op_sel_hi:[1,0]
	v_mov_b32_e32 v67, v70
	v_mov_b32_e32 v69, v71
	v_pk_add_f32 v[66:67], v[66:67], v[68:69]
	v_mul_f32_e32 v68, v31, v31
	v_mul_f32_e32 v70, v33, v33
	v_mul_f32_e32 v72, v28, v28
	v_mul_f32_e32 v73, v29, v29
	v_pk_fma_f32 v[68:69], v[30:31], v[30:31], v[68:69] op_sel_hi:[1,1,0]
	v_pk_fma_f32 v[70:71], v[32:33], v[32:33], v[70:71] op_sel_hi:[1,1,0]
	v_mov_b32_e32 v69, v72
	v_mov_b32_e32 v71, v73
	v_pk_add_f32 v[68:69], v[68:69], v[70:71]
	v_pk_mul_f32 v[70:71], v[22:23], v[22:23]
	v_pk_add_f32 v[66:67], v[66:67], v[68:69]
	v_pk_mul_f32 v[68:69], v[24:25], v[24:25]
	v_mul_f32_e32 v74, v14, v14
	v_pk_mov_b32 v[72:73], v[70:71], v[68:69] op_sel:[1,0]
	v_mov_b32_e32 v71, v69
	v_pk_add_f32 v[68:69], v[72:73], v[70:71]
	v_lshl_add_u64 v[70:71], v[156:157], 0, s[42:43]
	v_lshl_add_u64 v[72:73], v[70:71], 0, v[152:153]
	v_add_co_u32_e32 v70, vcc, s67, v72
	v_mul_f32_e32 v75, v15, v15
	s_nop 0
	v_addc_co_u32_e32 v71, vcc, 0, v73, vcc
	global_load_dwordx2 v[70:71], v[70:71], off offset:2048
	v_pk_add_f32 v[66:67], v[66:67], v[66:67] op_sel:[0,1] op_sel_hi:[1,0]
	v_pk_add_f32 v[68:69], v[68:69], v[68:69] op_sel:[0,1] op_sel_hi:[1,0]
	v_mov_b32_e32 v67, v74
	v_mov_b32_e32 v69, v75
	v_pk_add_f32 v[66:67], v[66:67], v[68:69]
	v_mul_f32_e32 v68, v19, v19
	v_mul_f32_e32 v74, v21, v21
	v_mul_f32_e32 v76, v16, v16
	v_mul_f32_e32 v77, v17, v17
	v_pk_fma_f32 v[68:69], v[18:19], v[18:19], v[68:69] op_sel_hi:[1,1,0]
	v_pk_fma_f32 v[74:75], v[20:21], v[20:21], v[74:75] op_sel_hi:[1,1,0]
	v_mov_b32_e32 v69, v76
	v_mov_b32_e32 v75, v77
	v_pk_add_f32 v[68:69], v[68:69], v[74:75]
	v_pk_mul_f32 v[74:75], v[10:11], v[10:11]
	v_pk_add_f32 v[66:67], v[66:67], v[68:69]
	v_pk_mul_f32 v[68:69], v[12:13], v[12:13]
	v_pk_add_f32 v[66:67], v[66:67], v[66:67] op_sel:[0,1] op_sel_hi:[1,0]
	v_pk_mov_b32 v[76:77], v[74:75], v[68:69] op_sel:[1,0]
	v_mov_b32_e32 v75, v69
	v_pk_add_f32 v[68:69], v[76:77], v[74:75]
	v_mul_f32_e32 v74, v2, v2
	v_mul_f32_e32 v75, v3, v3
	v_pk_add_f32 v[68:69], v[68:69], v[68:69] op_sel:[0,1] op_sel_hi:[1,0]
	v_mov_b32_e32 v67, v74
	v_mov_b32_e32 v69, v75
	v_pk_add_f32 v[66:67], v[66:67], v[68:69]
	v_mul_f32_e32 v68, v7, v7
	v_mul_f32_e32 v74, v9, v9
	v_mul_f32_e32 v76, v4, v4
	v_mul_f32_e32 v77, v5, v5
	v_pk_fma_f32 v[68:69], v[6:7], v[6:7], v[68:69] op_sel_hi:[1,1,0]
	v_pk_fma_f32 v[74:75], v[8:9], v[8:9], v[74:75] op_sel_hi:[1,1,0]
	v_mov_b32_e32 v69, v76
	v_mov_b32_e32 v75, v77
	v_pk_add_f32 v[68:69], v[68:69], v[74:75]
	v_mov_b32_e32 v92, v62
	v_pk_add_f32 v[66:67], v[66:67], v[68:69]
	v_and_b32_e32 v68, 64, v176
	v_add_u32_e32 v74, 64, v68
	v_lshl_add_u64 v[68:69], v[72:73], 0, s[22:23]
	global_load_dwordx2 v[72:73], v[68:69], off offset:32
	v_add_f32_e32 v66, v66, v67
	v_xor_b32_e32 v67, 16, v176
	v_cmp_lt_i32_e32 vcc, v67, v74
	global_load_dwordx2 v[76:77], v[68:69], off offset:416
	global_load_dwordx2 v[78:79], v[68:69], off offset:448
	global_load_dwordx2 v[80:81], v[68:69], off offset:480
	v_cndmask_b32_e32 v67, v176, v67, vcc
	v_lshlrev_b32_e32 v67, 2, v67
	ds_bpermute_b32 v67, v67, v66
	global_load_dwordx2 v[88:89], v[68:69], off offset:64
	v_mov_b32_e32 v93, v64
	v_mov_b32_e32 v64, v63
	s_add_i32 s40, s40, s33
	s_waitcnt lgkmcnt(0)
	v_add_f32_e32 v66, v66, v67
	v_xor_b32_e32 v67, 32, v176
	v_cmp_lt_i32_e32 vcc, v67, v74
	v_mov_b64_e32 v[74:75], s[10:11]
	v_mad_u64_u32 v[74:75], s[0:1], v154, s66, v[74:75]
	v_cndmask_b32_e32 v67, v176, v67, vcc
	v_lshlrev_b32_e32 v67, 2, v67
	ds_bpermute_b32 v67, v67, v66
	v_mad_i32_i24 v75, v155, s66, v75
	v_lshl_add_u64 v[74:75], v[74:75], 0, s[42:43]
	v_lshl_add_u64 v[84:85], v[74:75], 0, v[152:153]
	v_lshl_add_u64 v[74:75], v[84:85], 0, s[38:39]
	s_waitcnt lgkmcnt(0)
	v_add_f32_e32 v66, v66, v67
	v_fmamk_f32 v66, v66, 0x3b800000, v167
	v_mul_f32_e32 v67, 0x4b800000, v66
	v_cmp_gt_f32_e32 vcc, s65, v66
	s_cmpk_lt_i32 s40, 0x200
	s_waitcnt vmcnt(5)
	v_lshlrev_b32_e32 v82, 16, v70
	v_cndmask_b32_e32 v66, v66, v67, vcc
	v_rsq_f32_e32 v66, v66
	v_lshlrev_b32_e32 v83, 16, v71
	v_mul_f32_e32 v87, 0xbfb8aa3b, v83
	v_exp_f32_e32 v87, v87
	v_mul_f32_e32 v67, 0x45800000, v66
	v_cndmask_b32_e32 v66, v66, v67, vcc
	v_mul_f32_e32 v67, 0xbfb8aa3b, v82
	v_exp_f32_e32 v67, v67
	v_and_b32_e32 v70, 0xffff0000, v70
	v_and_b32_e32 v71, 0xffff0000, v71
	v_add_f32_e32 v62, 1.0, v87
	v_add_f32_e32 v67, 1.0, v67
	v_rcp_f32_e32 v86, v67
	v_mul_f32_e32 v67, 0xbfb8aa3b, v70
	v_rcp_f32_e32 v87, v62
	v_mul_f32_e32 v62, 0xbfb8aa3b, v71
	v_exp_f32_e32 v67, v67
	v_exp_f32_e32 v62, v62
	v_pk_mul_f32 v[82:83], v[86:87], v[82:83]
	v_add_co_u32_e32 v84, vcc, s68, v84
	v_add_f32_e32 v67, 1.0, v67
	v_add_f32_e32 v62, 1.0, v62
	v_rcp_f32_e32 v90, v67
	v_rcp_f32_e32 v91, v62
	v_pk_mul_f32 v[62:63], v[64:65], v[66:67] op_sel_hi:[1,0]
	v_pk_mul_f32 v[92:93], v[92:93], v[66:67] op_sel_hi:[1,0]
	v_addc_co_u32_e32 v85, vcc, 0, v85, vcc
	v_pk_mul_f32 v[64:65], v[90:91], v[70:71]
	v_pk_mul_f32 v[82:83], v[82:83], v[92:93]
	v_pk_mul_f32 v[62:63], v[64:65], v[62:63]
	v_and_b32_sdwa v64, v83, v177 dst_sel:DWORD dst_unused:UNUSED_PAD src0_sel:WORD_1 src1_sel:DWORD
	v_and_b32_sdwa v67, v63, v177 dst_sel:DWORD dst_unused:UNUSED_PAD src0_sel:WORD_1 src1_sel:DWORD
	v_and_b32_sdwa v70, v62, v177 dst_sel:DWORD dst_unused:UNUSED_PAD src0_sel:WORD_1 src1_sel:DWORD
	v_and_b32_sdwa v65, v82, v177 dst_sel:DWORD dst_unused:UNUSED_PAD src0_sel:WORD_1 src1_sel:DWORD
	v_add3_u32 v63, v63, v67, s63
	v_add3_u32 v62, v62, v70, s63
	v_add3_u32 v65, v82, v65, s63
	v_add3_u32 v64, v83, v64, s63
	v_and_b32_e32 v63, 0xffff0000, v63
	v_and_b32_e32 v62, 0xffff0000, v62
	v_or_b32_sdwa v63, v63, v64 dst_sel:DWORD dst_unused:UNUSED_PAD src0_sel:DWORD src1_sel:WORD_1
	v_or_b32_sdwa v62, v62, v65 dst_sel:DWORD dst_unused:UNUSED_PAD src0_sel:DWORD src1_sel:WORD_1
	global_load_dwordx2 v[64:65], v[68:69], off offset:96
	global_load_dwordx2 v[70:71], v[68:69], off offset:128
	global_load_dwordx2 v[212:213], v[68:69], off offset:160
	global_load_dwordx2 v[214:215], v[68:69], off offset:192
	global_load_dwordx2 v[216:217], v[68:69], off offset:224
	global_load_dwordx2 v[218:219], v[68:69], off offset:256
	global_load_dwordx2 v[220:221], v[68:69], off offset:288
	global_load_dwordx2 v[222:223], v[68:69], off offset:320
	global_load_dwordx2 v[224:225], v[68:69], off offset:352
	global_load_dwordx2 v[226:227], v[68:69], off offset:384
	s_waitcnt vmcnt(14)
	v_lshlrev_b32_e32 v82, 16, v72
	v_mul_f32_e32 v67, 0xbfb8aa3b, v82
	v_exp_f32_e32 v67, v67
	v_lshlrev_b32_e32 v83, 16, v73
	v_and_b32_e32 v72, 0xffff0000, v72
	global_store_dwordx2 v[84:85], v[62:63], off offset:2048
	v_add_f32_e32 v62, 1.0, v67
	v_mul_f32_e32 v63, 0xbfb8aa3b, v72
	v_mul_f32_e32 v67, 0xbfb8aa3b, v83
	v_exp_f32_e32 v63, v63
	v_exp_f32_e32 v67, v67
	v_and_b32_e32 v73, 0xffff0000, v73
	v_mov_b32_e32 v86, v58
	v_add_f32_e32 v63, 1.0, v63
	v_add_f32_e32 v58, 1.0, v67
	v_rcp_f32_e32 v84, v63
	v_rcp_f32_e32 v63, v58
	v_mul_f32_e32 v58, 0xbfb8aa3b, v73
	v_exp_f32_e32 v58, v58
	v_rcp_f32_e32 v62, v62
	v_mov_b32_e32 v87, v60
	v_pk_mul_f32 v[86:87], v[86:87], v[66:67] op_sel_hi:[1,0]
	v_add_f32_e32 v58, 1.0, v58
	v_rcp_f32_e32 v85, v58
	v_pk_mul_f32 v[62:63], v[62:63], v[82:83]
	v_mov_b32_e32 v60, v59
	v_pk_mul_f32 v[62:63], v[86:87], v[62:63]
	v_pk_mul_f32 v[58:59], v[60:61], v[66:67] op_sel_hi:[1,0]
	v_pk_mul_f32 v[60:61], v[84:85], v[72:73]
	v_mov_b32_e32 v82, v54
	v_pk_mul_f32 v[58:59], v[58:59], v[60:61]
	v_and_b32_sdwa v61, v62, v177 dst_sel:DWORD dst_unused:UNUSED_PAD src0_sel:WORD_1 src1_sel:DWORD
	v_add3_u32 v61, v62, v61, s63
	v_and_b32_sdwa v62, v59, v177 dst_sel:DWORD dst_unused:UNUSED_PAD src0_sel:WORD_1 src1_sel:DWORD
	v_and_b32_sdwa v60, v63, v177 dst_sel:DWORD dst_unused:UNUSED_PAD src0_sel:WORD_1 src1_sel:DWORD
	v_add3_u32 v59, v59, v62, s63
	v_add3_u32 v60, v63, v60, s63
	v_and_b32_e32 v59, 0xffff0000, v59
	v_or_b32_sdwa v59, v59, v60 dst_sel:DWORD dst_unused:UNUSED_PAD src0_sel:DWORD src1_sel:WORD_1
	s_waitcnt vmcnt(11)
	v_lshlrev_b32_e32 v60, 16, v88
	v_mul_f32_e32 v62, 0xbfb8aa3b, v60
	v_and_b32_sdwa v63, v58, v177 dst_sel:DWORD dst_unused:UNUSED_PAD src0_sel:WORD_1 src1_sel:DWORD
	v_exp_f32_e32 v62, v62
	v_add3_u32 v58, v58, v63, s63
	v_and_b32_e32 v58, 0xffff0000, v58
	v_or_b32_sdwa v58, v58, v61 dst_sel:DWORD dst_unused:UNUSED_PAD src0_sel:DWORD src1_sel:WORD_1
	global_store_dwordx2 v[74:75], v[58:59], off offset:32
	v_lshlrev_b32_e32 v61, 16, v89
	v_add_f32_e32 v58, 1.0, v62
	v_and_b32_e32 v62, 0xffff0000, v88
	v_mul_f32_e32 v59, 0xbfb8aa3b, v62
	v_mul_f32_e32 v67, 0xbfb8aa3b, v61
	v_exp_f32_e32 v59, v59
	v_exp_f32_e32 v67, v67
	v_and_b32_e32 v63, 0xffff0000, v89
	v_rcp_f32_e32 v58, v58
	v_add_f32_e32 v59, 1.0, v59
	v_add_f32_e32 v54, 1.0, v67
	v_rcp_f32_e32 v72, v59
	v_rcp_f32_e32 v59, v54
	v_mul_f32_e32 v54, 0xbfb8aa3b, v63
	v_exp_f32_e32 v54, v54
	v_mov_b32_e32 v83, v56
	v_pk_mul_f32 v[82:83], v[82:83], v[66:67] op_sel_hi:[1,0]
	v_pk_mul_f32 v[58:59], v[58:59], v[60:61]
	v_add_f32_e32 v54, 1.0, v54
	v_rcp_f32_e32 v73, v54
	v_mov_b32_e32 v56, v55
	v_pk_mul_f32 v[58:59], v[82:83], v[58:59]
	v_pk_mul_f32 v[54:55], v[56:57], v[66:67] op_sel_hi:[1,0]
	v_pk_mul_f32 v[56:57], v[72:73], v[62:63]
	s_waitcnt vmcnt(11)
	v_and_b32_e32 v60, 0xffff0000, v64
	v_pk_mul_f32 v[54:55], v[54:55], v[56:57]
	v_and_b32_sdwa v57, v58, v177 dst_sel:DWORD dst_unused:UNUSED_PAD src0_sel:WORD_1 src1_sel:DWORD
	v_add3_u32 v57, v58, v57, s63
	v_and_b32_sdwa v58, v55, v177 dst_sel:DWORD dst_unused:UNUSED_PAD src0_sel:WORD_1 src1_sel:DWORD
	v_and_b32_sdwa v56, v59, v177 dst_sel:DWORD dst_unused:UNUSED_PAD src0_sel:WORD_1 src1_sel:DWORD
	v_add3_u32 v55, v55, v58, s63
	v_add3_u32 v56, v59, v56, s63
	v_and_b32_e32 v55, 0xffff0000, v55
	v_or_b32_sdwa v55, v55, v56 dst_sel:DWORD dst_unused:UNUSED_PAD src0_sel:DWORD src1_sel:WORD_1
	v_lshlrev_b32_e32 v56, 16, v64
	v_mul_f32_e32 v58, 0xbfb8aa3b, v56
	v_and_b32_sdwa v59, v54, v177 dst_sel:DWORD dst_unused:UNUSED_PAD src0_sel:WORD_1 src1_sel:DWORD
	v_exp_f32_e32 v58, v58
	v_add3_u32 v54, v54, v59, s63
	v_and_b32_e32 v54, 0xffff0000, v54
	v_or_b32_sdwa v54, v54, v57 dst_sel:DWORD dst_unused:UNUSED_PAD src0_sel:DWORD src1_sel:WORD_1
	global_store_dwordx2 v[74:75], v[54:55], off offset:64
	v_add_f32_e32 v54, 1.0, v58
	v_lshlrev_b32_e32 v57, 16, v65
	v_mul_f32_e32 v55, 0xbfb8aa3b, v60
	v_mul_f32_e32 v62, 0xbfb8aa3b, v57
	v_exp_f32_e32 v55, v55
	v_exp_f32_e32 v63, v62
	v_and_b32_e32 v61, 0xffff0000, v65
	v_mov_b32_e32 v64, v50
	v_add_f32_e32 v55, 1.0, v55
	v_add_f32_e32 v50, 1.0, v63
	v_rcp_f32_e32 v62, v55
	v_rcp_f32_e32 v55, v50
	v_mul_f32_e32 v50, 0xbfb8aa3b, v61
	v_exp_f32_e32 v50, v50
	v_rcp_f32_e32 v54, v54
	v_mov_b32_e32 v65, v52
	v_pk_mul_f32 v[64:65], v[64:65], v[66:67] op_sel_hi:[1,0]
	v_add_f32_e32 v50, 1.0, v50
	v_rcp_f32_e32 v63, v50
	v_pk_mul_f32 v[54:55], v[54:55], v[56:57]
	v_mov_b32_e32 v52, v51
	v_pk_mul_f32 v[54:55], v[64:65], v[54:55]
	v_pk_mul_f32 v[50:51], v[52:53], v[66:67] op_sel_hi:[1,0]
	v_pk_mul_f32 v[52:53], v[62:63], v[60:61]
	s_waitcnt vmcnt(11)
	v_and_b32_e32 v56, 0xffff0000, v70
	v_pk_mul_f32 v[50:51], v[50:51], v[52:53]
	v_and_b32_sdwa v52, v55, v177 dst_sel:DWORD dst_unused:UNUSED_PAD src0_sel:WORD_1 src1_sel:DWORD
	v_and_b32_sdwa v53, v54, v177 dst_sel:DWORD dst_unused:UNUSED_PAD src0_sel:WORD_1 src1_sel:DWORD
	v_add3_u32 v53, v54, v53, s63
	v_add3_u32 v52, v55, v52, s63
	v_and_b32_sdwa v54, v51, v177 dst_sel:DWORD dst_unused:UNUSED_PAD src0_sel:WORD_1 src1_sel:DWORD
	v_and_b32_sdwa v55, v50, v177 dst_sel:DWORD dst_unused:UNUSED_PAD src0_sel:WORD_1 src1_sel:DWORD
	v_add3_u32 v51, v51, v54, s63
	v_add3_u32 v50, v50, v55, s63
	v_and_b32_e32 v51, 0xffff0000, v51
	v_and_b32_e32 v50, 0xffff0000, v50
	v_or_b32_sdwa v51, v51, v52 dst_sel:DWORD dst_unused:UNUSED_PAD src0_sel:DWORD src1_sel:WORD_1
	v_or_b32_sdwa v50, v50, v53 dst_sel:DWORD dst_unused:UNUSED_PAD src0_sel:DWORD src1_sel:WORD_1
	global_store_dwordx2 v[74:75], v[50:51], off offset:96
	v_lshlrev_b32_e32 v53, 16, v71
	v_mul_f32_e32 v55, 0xbfb8aa3b, v56
	v_mul_f32_e32 v60, 0xbfb8aa3b, v53
	v_exp_f32_e32 v55, v55
	v_exp_f32_e32 v61, v60
	v_lshlrev_b32_e32 v52, 16, v70
	v_mul_f32_e32 v54, 0xbfb8aa3b, v52
	v_and_b32_e32 v57, 0xffff0000, v71
	v_add_f32_e32 v55, 1.0, v55
	v_mov_b32_e32 v62, v46
	v_add_f32_e32 v46, 1.0, v61
	v_exp_f32_e32 v54, v54
	v_rcp_f32_e32 v60, v55
	v_rcp_f32_e32 v55, v46
	v_mul_f32_e32 v46, 0xbfb8aa3b, v57
	v_exp_f32_e32 v46, v46
	v_add_f32_e32 v54, 1.0, v54
	v_rcp_f32_e32 v54, v54
	v_mov_b32_e32 v63, v48
	v_add_f32_e32 v46, 1.0, v46
	v_rcp_f32_e32 v61, v46
	v_pk_mul_f32 v[62:63], v[62:63], v[66:67] op_sel_hi:[1,0]
	v_pk_mul_f32 v[52:53], v[54:55], v[52:53]
	v_mov_b32_e32 v48, v47
	v_pk_mul_f32 v[52:53], v[62:63], v[52:53]
	v_pk_mul_f32 v[46:47], v[48:49], v[66:67] op_sel_hi:[1,0]
	v_pk_mul_f32 v[48:49], v[60:61], v[56:57]
	v_mov_b32_e32 v60, v42
	v_pk_mul_f32 v[46:47], v[46:47], v[48:49]
	v_and_b32_sdwa v49, v52, v177 dst_sel:DWORD dst_unused:UNUSED_PAD src0_sel:WORD_1 src1_sel:DWORD
	v_add3_u32 v55, v52, v49, s63
	v_and_b32_sdwa v49, v47, v177 dst_sel:DWORD dst_unused:UNUSED_PAD src0_sel:WORD_1 src1_sel:DWORD
	v_and_b32_sdwa v48, v53, v177 dst_sel:DWORD dst_unused:UNUSED_PAD src0_sel:WORD_1 src1_sel:DWORD
	v_add3_u32 v47, v47, v49, s63
	v_add3_u32 v48, v53, v48, s63
	v_and_b32_sdwa v52, v46, v177 dst_sel:DWORD dst_unused:UNUSED_PAD src0_sel:WORD_1 src1_sel:DWORD
	v_and_b32_e32 v47, 0xffff0000, v47
	v_add3_u32 v46, v46, v52, s63
	v_or_b32_sdwa v47, v47, v48 dst_sel:DWORD dst_unused:UNUSED_PAD src0_sel:DWORD src1_sel:WORD_1
	s_waitcnt vmcnt(11)
	v_lshlrev_b32_e32 v54, 16, v212
	v_mul_f32_e32 v56, 0xbfb8aa3b, v54
	v_exp_f32_e32 v56, v56
	v_and_b32_e32 v46, 0xffff0000, v46
	v_or_b32_sdwa v46, v46, v55 dst_sel:DWORD dst_unused:UNUSED_PAD src0_sel:DWORD src1_sel:WORD_1
	global_store_dwordx2 v[74:75], v[46:47], off offset:128
	v_lshlrev_b32_e32 v55, 16, v213
	v_add_f32_e32 v46, 1.0, v56
	v_and_b32_e32 v56, 0xffff0000, v212
	v_mul_f32_e32 v47, 0xbfb8aa3b, v56
	v_mul_f32_e32 v58, 0xbfb8aa3b, v55
	v_exp_f32_e32 v47, v47
	v_and_b32_e32 v57, 0xffff0000, v213
	v_exp_f32_e32 v59, v58
	v_rcp_f32_e32 v46, v46
	v_add_f32_e32 v47, 1.0, v47
	v_rcp_f32_e32 v58, v47
	v_add_f32_e32 v42, 1.0, v59
	v_rcp_f32_e32 v47, v42
	v_mul_f32_e32 v42, 0xbfb8aa3b, v57
	v_exp_f32_e32 v42, v42
	v_mov_b32_e32 v61, v44
	v_pk_mul_f32 v[60:61], v[60:61], v[66:67] op_sel_hi:[1,0]
	v_pk_mul_f32 v[46:47], v[46:47], v[54:55]
	v_add_f32_e32 v42, 1.0, v42
	v_rcp_f32_e32 v59, v42
	v_mov_b32_e32 v44, v43
	v_pk_mul_f32 v[46:47], v[60:61], v[46:47]
	v_pk_mul_f32 v[42:43], v[44:45], v[66:67] op_sel_hi:[1,0]
	v_pk_mul_f32 v[44:45], v[58:59], v[56:57]
	v_mov_b32_e32 v54, v38
	v_pk_mul_f32 v[42:43], v[42:43], v[44:45]
	v_and_b32_sdwa v45, v46, v177 dst_sel:DWORD dst_unused:UNUSED_PAD src0_sel:WORD_1 src1_sel:DWORD
	v_add3_u32 v45, v46, v45, s63
	v_and_b32_sdwa v46, v43, v177 dst_sel:DWORD dst_unused:UNUSED_PAD src0_sel:WORD_1 src1_sel:DWORD
	v_and_b32_sdwa v44, v47, v177 dst_sel:DWORD dst_unused:UNUSED_PAD src0_sel:WORD_1 src1_sel:DWORD
	v_add3_u32 v43, v43, v46, s63
	v_add3_u32 v44, v47, v44, s63
	v_and_b32_e32 v43, 0xffff0000, v43
	v_or_b32_sdwa v43, v43, v44 dst_sel:DWORD dst_unused:UNUSED_PAD src0_sel:DWORD src1_sel:WORD_1
	s_waitcnt vmcnt(11)
	v_lshlrev_b32_e32 v44, 16, v214
	v_mul_f32_e32 v46, 0xbfb8aa3b, v44
	v_and_b32_sdwa v47, v42, v177 dst_sel:DWORD dst_unused:UNUSED_PAD src0_sel:WORD_1 src1_sel:DWORD
	v_exp_f32_e32 v46, v46
	v_add3_u32 v42, v42, v47, s63
	v_and_b32_e32 v42, 0xffff0000, v42
	v_or_b32_sdwa v42, v42, v45 dst_sel:DWORD dst_unused:UNUSED_PAD src0_sel:DWORD src1_sel:WORD_1
	global_store_dwordx2 v[74:75], v[42:43], off offset:160
	v_lshlrev_b32_e32 v45, 16, v215
	v_add_f32_e32 v42, 1.0, v46
	v_and_b32_e32 v46, 0xffff0000, v214
	v_mul_f32_e32 v43, 0xbfb8aa3b, v46
	v_mul_f32_e32 v50, 0xbfb8aa3b, v45
	v_exp_f32_e32 v43, v43
	v_and_b32_e32 v47, 0xffff0000, v215
	v_exp_f32_e32 v51, v50
	v_rcp_f32_e32 v42, v42
	v_add_f32_e32 v43, 1.0, v43
	v_rcp_f32_e32 v50, v43
	v_add_f32_e32 v38, 1.0, v51
	v_rcp_f32_e32 v43, v38
	v_mul_f32_e32 v38, 0xbfb8aa3b, v47
	v_exp_f32_e32 v38, v38
	v_mov_b32_e32 v55, v40
	v_pk_mul_f32 v[54:55], v[54:55], v[66:67] op_sel_hi:[1,0]
	v_pk_mul_f32 v[42:43], v[42:43], v[44:45]
	v_add_f32_e32 v38, 1.0, v38
	v_rcp_f32_e32 v51, v38
	v_mov_b32_e32 v40, v39
	v_pk_mul_f32 v[42:43], v[54:55], v[42:43]
	v_pk_mul_f32 v[38:39], v[40:41], v[66:67] op_sel_hi:[1,0]
	v_pk_mul_f32 v[40:41], v[50:51], v[46:47]
	s_waitcnt vmcnt(11)
	v_and_b32_e32 v44, 0xffff0000, v216
	v_pk_mul_f32 v[38:39], v[38:39], v[40:41]
	v_and_b32_sdwa v41, v42, v177 dst_sel:DWORD dst_unused:UNUSED_PAD src0_sel:WORD_1 src1_sel:DWORD
	v_add3_u32 v41, v42, v41, s63
	v_and_b32_sdwa v42, v39, v177 dst_sel:DWORD dst_unused:UNUSED_PAD src0_sel:WORD_1 src1_sel:DWORD
	v_and_b32_sdwa v40, v43, v177 dst_sel:DWORD dst_unused:UNUSED_PAD src0_sel:WORD_1 src1_sel:DWORD
	v_add3_u32 v39, v39, v42, s63
	v_add3_u32 v40, v43, v40, s63
	v_and_b32_e32 v39, 0xffff0000, v39
	v_or_b32_sdwa v39, v39, v40 dst_sel:DWORD dst_unused:UNUSED_PAD src0_sel:DWORD src1_sel:WORD_1
	v_lshlrev_b32_e32 v40, 16, v216
	v_mul_f32_e32 v42, 0xbfb8aa3b, v40
	v_and_b32_sdwa v43, v38, v177 dst_sel:DWORD dst_unused:UNUSED_PAD src0_sel:WORD_1 src1_sel:DWORD
	v_exp_f32_e32 v42, v42
	v_add3_u32 v38, v38, v43, s63
	v_and_b32_e32 v38, 0xffff0000, v38
	v_or_b32_sdwa v38, v38, v41 dst_sel:DWORD dst_unused:UNUSED_PAD src0_sel:DWORD src1_sel:WORD_1
	global_store_dwordx2 v[74:75], v[38:39], off offset:192
	v_add_f32_e32 v38, 1.0, v42
	v_lshlrev_b32_e32 v41, 16, v217
	v_mul_f32_e32 v39, 0xbfb8aa3b, v44
	v_mul_f32_e32 v46, 0xbfb8aa3b, v41
	v_exp_f32_e32 v39, v39
	v_exp_f32_e32 v47, v46
	v_and_b32_e32 v45, 0xffff0000, v217
	v_mov_b32_e32 v48, v34
	v_add_f32_e32 v39, 1.0, v39
	v_add_f32_e32 v34, 1.0, v47
	v_rcp_f32_e32 v46, v39
	v_rcp_f32_e32 v39, v34
	v_mul_f32_e32 v34, 0xbfb8aa3b, v45
	v_exp_f32_e32 v34, v34
	v_rcp_f32_e32 v38, v38
	v_mov_b32_e32 v49, v36
	v_pk_mul_f32 v[48:49], v[48:49], v[66:67] op_sel_hi:[1,0]
	v_add_f32_e32 v34, 1.0, v34
	v_rcp_f32_e32 v47, v34
	v_pk_mul_f32 v[38:39], v[38:39], v[40:41]
	v_mov_b32_e32 v36, v35
	v_pk_mul_f32 v[38:39], v[48:49], v[38:39]
	v_pk_mul_f32 v[34:35], v[36:37], v[66:67] op_sel_hi:[1,0]
	v_pk_mul_f32 v[36:37], v[46:47], v[44:45]
	s_waitcnt vmcnt(11)
	v_and_b32_e32 v40, 0xffff0000, v218
	v_pk_mul_f32 v[34:35], v[34:35], v[36:37]
	v_and_b32_sdwa v36, v39, v177 dst_sel:DWORD dst_unused:UNUSED_PAD src0_sel:WORD_1 src1_sel:DWORD
	v_and_b32_sdwa v37, v38, v177 dst_sel:DWORD dst_unused:UNUSED_PAD src0_sel:WORD_1 src1_sel:DWORD
	v_add3_u32 v37, v38, v37, s63
	v_add3_u32 v36, v39, v36, s63
	v_and_b32_sdwa v38, v35, v177 dst_sel:DWORD dst_unused:UNUSED_PAD src0_sel:WORD_1 src1_sel:DWORD
	v_and_b32_sdwa v39, v34, v177 dst_sel:DWORD dst_unused:UNUSED_PAD src0_sel:WORD_1 src1_sel:DWORD
	v_add3_u32 v35, v35, v38, s63
	v_add3_u32 v34, v34, v39, s63
	v_and_b32_e32 v35, 0xffff0000, v35
	v_and_b32_e32 v34, 0xffff0000, v34
	v_or_b32_sdwa v35, v35, v36 dst_sel:DWORD dst_unused:UNUSED_PAD src0_sel:DWORD src1_sel:WORD_1
	v_or_b32_sdwa v34, v34, v37 dst_sel:DWORD dst_unused:UNUSED_PAD src0_sel:DWORD src1_sel:WORD_1
	global_store_dwordx2 v[74:75], v[34:35], off offset:224
	v_lshlrev_b32_e32 v37, 16, v219
	v_mul_f32_e32 v39, 0xbfb8aa3b, v40
	v_mul_f32_e32 v44, 0xbfb8aa3b, v37
	v_exp_f32_e32 v39, v39
	v_exp_f32_e32 v45, v44
	v_lshlrev_b32_e32 v36, 16, v218
	v_mul_f32_e32 v38, 0xbfb8aa3b, v36
	v_and_b32_e32 v41, 0xffff0000, v219
	v_add_f32_e32 v39, 1.0, v39
	v_mov_b32_e32 v46, v30
	v_add_f32_e32 v30, 1.0, v45
	v_exp_f32_e32 v38, v38
	v_rcp_f32_e32 v44, v39
	v_rcp_f32_e32 v39, v30
	v_mul_f32_e32 v30, 0xbfb8aa3b, v41
	v_exp_f32_e32 v30, v30
	v_add_f32_e32 v38, 1.0, v38
	v_rcp_f32_e32 v38, v38
	v_mov_b32_e32 v47, v32
	v_add_f32_e32 v30, 1.0, v30
	v_rcp_f32_e32 v45, v30
	v_pk_mul_f32 v[46:47], v[46:47], v[66:67] op_sel_hi:[1,0]
	v_pk_mul_f32 v[36:37], v[38:39], v[36:37]
	v_mov_b32_e32 v32, v31
	v_pk_mul_f32 v[36:37], v[46:47], v[36:37]
	v_pk_mul_f32 v[30:31], v[32:33], v[66:67] op_sel_hi:[1,0]
	v_pk_mul_f32 v[32:33], v[44:45], v[40:41]
	v_mov_b32_e32 v44, v26
	v_pk_mul_f32 v[30:31], v[30:31], v[32:33]
	v_and_b32_sdwa v33, v36, v177 dst_sel:DWORD dst_unused:UNUSED_PAD src0_sel:WORD_1 src1_sel:DWORD
	v_add3_u32 v39, v36, v33, s63
	v_and_b32_sdwa v33, v31, v177 dst_sel:DWORD dst_unused:UNUSED_PAD src0_sel:WORD_1 src1_sel:DWORD
	v_and_b32_sdwa v32, v37, v177 dst_sel:DWORD dst_unused:UNUSED_PAD src0_sel:WORD_1 src1_sel:DWORD
	v_add3_u32 v31, v31, v33, s63
	v_add3_u32 v32, v37, v32, s63
	v_and_b32_sdwa v36, v30, v177 dst_sel:DWORD dst_unused:UNUSED_PAD src0_sel:WORD_1 src1_sel:DWORD
	v_and_b32_e32 v31, 0xffff0000, v31
	v_add3_u32 v30, v30, v36, s63
	v_or_b32_sdwa v31, v31, v32 dst_sel:DWORD dst_unused:UNUSED_PAD src0_sel:DWORD src1_sel:WORD_1
	s_waitcnt vmcnt(11)
	v_lshlrev_b32_e32 v38, 16, v220
	v_mul_f32_e32 v40, 0xbfb8aa3b, v38
	v_exp_f32_e32 v40, v40
	v_and_b32_e32 v30, 0xffff0000, v30
	v_or_b32_sdwa v30, v30, v39 dst_sel:DWORD dst_unused:UNUSED_PAD src0_sel:DWORD src1_sel:WORD_1
	global_store_dwordx2 v[74:75], v[30:31], off offset:256
	v_lshlrev_b32_e32 v39, 16, v221
	v_add_f32_e32 v30, 1.0, v40
	v_and_b32_e32 v40, 0xffff0000, v220
	v_mul_f32_e32 v31, 0xbfb8aa3b, v40
	v_mul_f32_e32 v42, 0xbfb8aa3b, v39
	v_exp_f32_e32 v31, v31
	v_and_b32_e32 v41, 0xffff0000, v221
	v_exp_f32_e32 v43, v42
	v_rcp_f32_e32 v30, v30
	v_add_f32_e32 v31, 1.0, v31
	v_rcp_f32_e32 v42, v31
	v_add_f32_e32 v26, 1.0, v43
	v_rcp_f32_e32 v31, v26
	v_mul_f32_e32 v26, 0xbfb8aa3b, v41
	v_exp_f32_e32 v26, v26
	v_mov_b32_e32 v45, v28
	v_pk_mul_f32 v[44:45], v[44:45], v[66:67] op_sel_hi:[1,0]
	v_pk_mul_f32 v[30:31], v[30:31], v[38:39]
	v_add_f32_e32 v26, 1.0, v26
	v_rcp_f32_e32 v43, v26
	v_mov_b32_e32 v28, v27
	v_pk_mul_f32 v[30:31], v[44:45], v[30:31]
	v_pk_mul_f32 v[26:27], v[28:29], v[66:67] op_sel_hi:[1,0]
	v_pk_mul_f32 v[28:29], v[42:43], v[40:41]
	v_mov_b32_e32 v38, v22
	v_pk_mul_f32 v[26:27], v[26:27], v[28:29]
	v_and_b32_sdwa v29, v30, v177 dst_sel:DWORD dst_unused:UNUSED_PAD src0_sel:WORD_1 src1_sel:DWORD
	v_add3_u32 v29, v30, v29, s63
	v_and_b32_sdwa v30, v27, v177 dst_sel:DWORD dst_unused:UNUSED_PAD src0_sel:WORD_1 src1_sel:DWORD
	v_and_b32_sdwa v28, v31, v177 dst_sel:DWORD dst_unused:UNUSED_PAD src0_sel:WORD_1 src1_sel:DWORD
	v_add3_u32 v27, v27, v30, s63
	v_add3_u32 v28, v31, v28, s63
	v_and_b32_e32 v27, 0xffff0000, v27
	v_or_b32_sdwa v27, v27, v28 dst_sel:DWORD dst_unused:UNUSED_PAD src0_sel:DWORD src1_sel:WORD_1
	s_waitcnt vmcnt(11)
	v_lshlrev_b32_e32 v28, 16, v222
	v_mul_f32_e32 v30, 0xbfb8aa3b, v28
	v_and_b32_sdwa v31, v26, v177 dst_sel:DWORD dst_unused:UNUSED_PAD src0_sel:WORD_1 src1_sel:DWORD
	v_exp_f32_e32 v30, v30
	v_add3_u32 v26, v26, v31, s63
	v_and_b32_e32 v26, 0xffff0000, v26
	v_or_b32_sdwa v26, v26, v29 dst_sel:DWORD dst_unused:UNUSED_PAD src0_sel:DWORD src1_sel:WORD_1
	global_store_dwordx2 v[74:75], v[26:27], off offset:288
	v_lshlrev_b32_e32 v29, 16, v223
	v_add_f32_e32 v26, 1.0, v30
	v_and_b32_e32 v30, 0xffff0000, v222
	v_mul_f32_e32 v27, 0xbfb8aa3b, v30
	v_mul_f32_e32 v34, 0xbfb8aa3b, v29
	v_exp_f32_e32 v27, v27
	v_and_b32_e32 v31, 0xffff0000, v223
	v_exp_f32_e32 v35, v34
	v_rcp_f32_e32 v26, v26
	v_add_f32_e32 v27, 1.0, v27
	v_rcp_f32_e32 v34, v27
	v_add_f32_e32 v22, 1.0, v35
	v_rcp_f32_e32 v27, v22
	v_mul_f32_e32 v22, 0xbfb8aa3b, v31
	v_exp_f32_e32 v22, v22
	v_mov_b32_e32 v39, v24
	v_pk_mul_f32 v[38:39], v[38:39], v[66:67] op_sel_hi:[1,0]
	v_pk_mul_f32 v[26:27], v[26:27], v[28:29]
	v_add_f32_e32 v22, 1.0, v22
	v_rcp_f32_e32 v35, v22
	v_mov_b32_e32 v24, v23
	v_pk_mul_f32 v[26:27], v[38:39], v[26:27]
	v_pk_mul_f32 v[22:23], v[24:25], v[66:67] op_sel_hi:[1,0]
	v_pk_mul_f32 v[24:25], v[34:35], v[30:31]
	v_mov_b32_e32 v30, v18
	v_pk_mul_f32 v[22:23], v[22:23], v[24:25]
	v_and_b32_sdwa v25, v26, v177 dst_sel:DWORD dst_unused:UNUSED_PAD src0_sel:WORD_1 src1_sel:DWORD
	v_add3_u32 v25, v26, v25, s63
	v_and_b32_sdwa v26, v23, v177 dst_sel:DWORD dst_unused:UNUSED_PAD src0_sel:WORD_1 src1_sel:DWORD
	v_and_b32_sdwa v24, v27, v177 dst_sel:DWORD dst_unused:UNUSED_PAD src0_sel:WORD_1 src1_sel:DWORD
	v_add3_u32 v23, v23, v26, s63
	v_add3_u32 v24, v27, v24, s63
	v_and_b32_e32 v23, 0xffff0000, v23
	v_or_b32_sdwa v23, v23, v24 dst_sel:DWORD dst_unused:UNUSED_PAD src0_sel:DWORD src1_sel:WORD_1
	s_waitcnt vmcnt(11)
	v_lshlrev_b32_e32 v24, 16, v224
	v_mul_f32_e32 v26, 0xbfb8aa3b, v24
	v_and_b32_sdwa v27, v22, v177 dst_sel:DWORD dst_unused:UNUSED_PAD src0_sel:WORD_1 src1_sel:DWORD
	v_exp_f32_e32 v26, v26
	v_add3_u32 v22, v22, v27, s63
	v_and_b32_e32 v22, 0xffff0000, v22
	v_or_b32_sdwa v22, v22, v25 dst_sel:DWORD dst_unused:UNUSED_PAD src0_sel:DWORD src1_sel:WORD_1
	global_store_dwordx2 v[74:75], v[22:23], off offset:320
	v_lshlrev_b32_e32 v25, 16, v225
	v_add_f32_e32 v22, 1.0, v26
	v_and_b32_e32 v26, 0xffff0000, v224
	v_mul_f32_e32 v23, 0xbfb8aa3b, v26
	v_mul_f32_e32 v28, 0xbfb8aa3b, v25
	v_exp_f32_e32 v23, v23
	v_exp_f32_e32 v29, v28
	v_and_b32_e32 v27, 0xffff0000, v225
	v_rcp_f32_e32 v22, v22
	v_add_f32_e32 v23, 1.0, v23
	v_add_f32_e32 v18, 1.0, v29
	v_rcp_f32_e32 v28, v23
	v_rcp_f32_e32 v23, v18
	v_mul_f32_e32 v18, 0xbfb8aa3b, v27
	v_exp_f32_e32 v18, v18
	v_mov_b32_e32 v31, v20
	v_pk_mul_f32 v[30:31], v[30:31], v[66:67] op_sel_hi:[1,0]
	v_pk_mul_f32 v[22:23], v[22:23], v[24:25]
	v_add_f32_e32 v18, 1.0, v18
	v_rcp_f32_e32 v29, v18
	v_mov_b32_e32 v20, v19
	v_pk_mul_f32 v[22:23], v[30:31], v[22:23]
	v_pk_mul_f32 v[18:19], v[20:21], v[66:67] op_sel_hi:[1,0]
	v_pk_mul_f32 v[20:21], v[28:29], v[26:27]
	v_mov_b32_e32 v26, v14
	v_pk_mul_f32 v[18:19], v[18:19], v[20:21]
	v_and_b32_sdwa v21, v22, v177 dst_sel:DWORD dst_unused:UNUSED_PAD src0_sel:WORD_1 src1_sel:DWORD
	v_add3_u32 v21, v22, v21, s63
	v_and_b32_sdwa v22, v19, v177 dst_sel:DWORD dst_unused:UNUSED_PAD src0_sel:WORD_1 src1_sel:DWORD
	v_and_b32_sdwa v20, v23, v177 dst_sel:DWORD dst_unused:UNUSED_PAD src0_sel:WORD_1 src1_sel:DWORD
	v_add3_u32 v19, v19, v22, s63
	v_add3_u32 v20, v23, v20, s63
	v_and_b32_e32 v19, 0xffff0000, v19
	v_or_b32_sdwa v19, v19, v20 dst_sel:DWORD dst_unused:UNUSED_PAD src0_sel:DWORD src1_sel:WORD_1
	s_waitcnt vmcnt(11)
	v_lshlrev_b32_e32 v20, 16, v226
	v_mul_f32_e32 v22, 0xbfb8aa3b, v20
	v_and_b32_sdwa v23, v18, v177 dst_sel:DWORD dst_unused:UNUSED_PAD src0_sel:WORD_1 src1_sel:DWORD
	v_exp_f32_e32 v22, v22
	v_add3_u32 v18, v18, v23, s63
	v_and_b32_e32 v18, 0xffff0000, v18
	v_or_b32_sdwa v18, v18, v21 dst_sel:DWORD dst_unused:UNUSED_PAD src0_sel:DWORD src1_sel:WORD_1
	global_store_dwordx2 v[74:75], v[18:19], off offset:352
	v_lshlrev_b32_e32 v21, 16, v227
	v_add_f32_e32 v18, 1.0, v22
	v_and_b32_e32 v22, 0xffff0000, v226
	v_mul_f32_e32 v19, 0xbfb8aa3b, v22
	v_mul_f32_e32 v24, 0xbfb8aa3b, v21
	v_exp_f32_e32 v19, v19
	v_exp_f32_e32 v25, v24
	v_and_b32_e32 v23, 0xffff0000, v227
	v_rcp_f32_e32 v18, v18
	v_add_f32_e32 v19, 1.0, v19
	v_add_f32_e32 v14, 1.0, v25
	v_rcp_f32_e32 v24, v19
	v_rcp_f32_e32 v19, v14
	v_mul_f32_e32 v14, 0xbfb8aa3b, v23
	v_exp_f32_e32 v14, v14
	v_mov_b32_e32 v27, v16
	v_pk_mul_f32 v[26:27], v[26:27], v[66:67] op_sel_hi:[1,0]
	v_pk_mul_f32 v[18:19], v[18:19], v[20:21]
	v_add_f32_e32 v14, 1.0, v14
	v_rcp_f32_e32 v25, v14
	v_mov_b32_e32 v16, v15
	v_pk_mul_f32 v[18:19], v[26:27], v[18:19]
	v_pk_mul_f32 v[14:15], v[16:17], v[66:67] op_sel_hi:[1,0]
	v_pk_mul_f32 v[16:17], v[24:25], v[22:23]
	v_mov_b32_e32 v22, v10
	v_pk_mul_f32 v[14:15], v[14:15], v[16:17]
	v_and_b32_sdwa v17, v18, v177 dst_sel:DWORD dst_unused:UNUSED_PAD src0_sel:WORD_1 src1_sel:DWORD
	v_add3_u32 v17, v18, v17, s63
	v_and_b32_sdwa v18, v15, v177 dst_sel:DWORD dst_unused:UNUSED_PAD src0_sel:WORD_1 src1_sel:DWORD
	v_and_b32_sdwa v16, v19, v177 dst_sel:DWORD dst_unused:UNUSED_PAD src0_sel:WORD_1 src1_sel:DWORD
	v_add3_u32 v15, v15, v18, s63
	v_add3_u32 v16, v19, v16, s63
	v_and_b32_e32 v15, 0xffff0000, v15
	v_or_b32_sdwa v15, v15, v16 dst_sel:DWORD dst_unused:UNUSED_PAD src0_sel:DWORD src1_sel:WORD_1
	v_lshlrev_b32_e32 v16, 16, v76
	v_mul_f32_e32 v18, 0xbfb8aa3b, v16
	v_and_b32_sdwa v19, v14, v177 dst_sel:DWORD dst_unused:UNUSED_PAD src0_sel:WORD_1 src1_sel:DWORD
	v_exp_f32_e32 v18, v18
	v_add3_u32 v14, v14, v19, s63
	v_and_b32_e32 v14, 0xffff0000, v14
	v_or_b32_sdwa v14, v14, v17 dst_sel:DWORD dst_unused:UNUSED_PAD src0_sel:DWORD src1_sel:WORD_1
	global_store_dwordx2 v[74:75], v[14:15], off offset:384
	v_lshlrev_b32_e32 v17, 16, v77
	v_add_f32_e32 v14, 1.0, v18
	v_and_b32_e32 v18, 0xffff0000, v76
	v_mul_f32_e32 v15, 0xbfb8aa3b, v18
	v_mul_f32_e32 v20, 0xbfb8aa3b, v17
	v_exp_f32_e32 v15, v15
	v_exp_f32_e32 v21, v20
	v_and_b32_e32 v19, 0xffff0000, v77
	v_rcp_f32_e32 v14, v14
	v_add_f32_e32 v15, 1.0, v15
	v_add_f32_e32 v10, 1.0, v21
	v_rcp_f32_e32 v20, v15
	v_rcp_f32_e32 v15, v10
	v_mul_f32_e32 v10, 0xbfb8aa3b, v19
	v_exp_f32_e32 v10, v10
	v_mov_b32_e32 v23, v12
	v_pk_mul_f32 v[22:23], v[22:23], v[66:67] op_sel_hi:[1,0]
	v_pk_mul_f32 v[14:15], v[14:15], v[16:17]
	v_add_f32_e32 v10, 1.0, v10
	v_rcp_f32_e32 v21, v10
	v_mov_b32_e32 v12, v11
	v_pk_mul_f32 v[14:15], v[22:23], v[14:15]
	v_pk_mul_f32 v[10:11], v[12:13], v[66:67] op_sel_hi:[1,0]
	v_pk_mul_f32 v[12:13], v[20:21], v[18:19]
	v_mov_b32_e32 v18, v6
	v_pk_mul_f32 v[10:11], v[10:11], v[12:13]
	v_and_b32_sdwa v13, v14, v177 dst_sel:DWORD dst_unused:UNUSED_PAD src0_sel:WORD_1 src1_sel:DWORD
	v_add3_u32 v13, v14, v13, s63
	v_and_b32_sdwa v14, v11, v177 dst_sel:DWORD dst_unused:UNUSED_PAD src0_sel:WORD_1 src1_sel:DWORD
	v_and_b32_sdwa v12, v15, v177 dst_sel:DWORD dst_unused:UNUSED_PAD src0_sel:WORD_1 src1_sel:DWORD
	v_add3_u32 v11, v11, v14, s63
	v_add3_u32 v12, v15, v12, s63
	v_and_b32_e32 v11, 0xffff0000, v11
	v_or_b32_sdwa v11, v11, v12 dst_sel:DWORD dst_unused:UNUSED_PAD src0_sel:DWORD src1_sel:WORD_1
	v_lshlrev_b32_e32 v12, 16, v78
	v_mul_f32_e32 v14, 0xbfb8aa3b, v12
	v_and_b32_sdwa v15, v10, v177 dst_sel:DWORD dst_unused:UNUSED_PAD src0_sel:WORD_1 src1_sel:DWORD
	v_exp_f32_e32 v14, v14
	v_add3_u32 v10, v10, v15, s63
	v_and_b32_e32 v10, 0xffff0000, v10
	v_or_b32_sdwa v10, v10, v13 dst_sel:DWORD dst_unused:UNUSED_PAD src0_sel:DWORD src1_sel:WORD_1
	global_store_dwordx2 v[74:75], v[10:11], off offset:416
	v_lshlrev_b32_e32 v13, 16, v79
	v_add_f32_e32 v10, 1.0, v14
	v_and_b32_e32 v14, 0xffff0000, v78
	v_mul_f32_e32 v11, 0xbfb8aa3b, v14
	v_mul_f32_e32 v16, 0xbfb8aa3b, v13
	v_exp_f32_e32 v11, v11
	v_exp_f32_e32 v17, v16
	v_and_b32_e32 v15, 0xffff0000, v79
	v_rcp_f32_e32 v10, v10
	v_add_f32_e32 v11, 1.0, v11
	v_add_f32_e32 v6, 1.0, v17
	v_rcp_f32_e32 v16, v11
	v_rcp_f32_e32 v11, v6
	v_mul_f32_e32 v6, 0xbfb8aa3b, v15
	v_exp_f32_e32 v6, v6
	v_mov_b32_e32 v19, v8
	v_pk_mul_f32 v[18:19], v[18:19], v[66:67] op_sel_hi:[1,0]
	v_pk_mul_f32 v[10:11], v[10:11], v[12:13]
	v_add_f32_e32 v6, 1.0, v6
	v_rcp_f32_e32 v17, v6
	v_mov_b32_e32 v8, v7
	v_pk_mul_f32 v[10:11], v[18:19], v[10:11]
	v_pk_mul_f32 v[6:7], v[8:9], v[66:67] op_sel_hi:[1,0]
	v_pk_mul_f32 v[8:9], v[16:17], v[14:15]
	v_mov_b32_e32 v14, v2
	v_pk_mul_f32 v[6:7], v[6:7], v[8:9]
	v_and_b32_sdwa v9, v10, v177 dst_sel:DWORD dst_unused:UNUSED_PAD src0_sel:WORD_1 src1_sel:DWORD
	v_add3_u32 v9, v10, v9, s63
	v_and_b32_sdwa v10, v7, v177 dst_sel:DWORD dst_unused:UNUSED_PAD src0_sel:WORD_1 src1_sel:DWORD
	v_and_b32_sdwa v8, v11, v177 dst_sel:DWORD dst_unused:UNUSED_PAD src0_sel:WORD_1 src1_sel:DWORD
	v_add3_u32 v7, v7, v10, s63
	v_add3_u32 v8, v11, v8, s63
	v_and_b32_e32 v7, 0xffff0000, v7
	v_or_b32_sdwa v7, v7, v8 dst_sel:DWORD dst_unused:UNUSED_PAD src0_sel:DWORD src1_sel:WORD_1
	v_lshlrev_b32_e32 v8, 16, v80
	v_mul_f32_e32 v10, 0xbfb8aa3b, v8
	v_and_b32_sdwa v11, v6, v177 dst_sel:DWORD dst_unused:UNUSED_PAD src0_sel:WORD_1 src1_sel:DWORD
	v_exp_f32_e32 v10, v10
	v_add3_u32 v6, v6, v11, s63
	v_and_b32_e32 v6, 0xffff0000, v6
	v_or_b32_sdwa v6, v6, v9 dst_sel:DWORD dst_unused:UNUSED_PAD src0_sel:DWORD src1_sel:WORD_1
	global_store_dwordx2 v[74:75], v[6:7], off offset:448
	v_lshlrev_b32_e32 v9, 16, v81
	v_add_f32_e32 v6, 1.0, v10
	v_and_b32_e32 v10, 0xffff0000, v80
	v_mul_f32_e32 v7, 0xbfb8aa3b, v10
	v_mul_f32_e32 v12, 0xbfb8aa3b, v9
	v_exp_f32_e32 v7, v7
	v_exp_f32_e32 v13, v12
	v_and_b32_e32 v11, 0xffff0000, v81
	v_rcp_f32_e32 v6, v6
	v_add_f32_e32 v7, 1.0, v7
	v_add_f32_e32 v2, 1.0, v13
	v_rcp_f32_e32 v12, v7
	v_rcp_f32_e32 v7, v2
	v_mul_f32_e32 v2, 0xbfb8aa3b, v11
	v_exp_f32_e32 v2, v2
	v_mov_b32_e32 v15, v4
	v_pk_mul_f32 v[14:15], v[14:15], v[66:67] op_sel_hi:[1,0]
	v_pk_mul_f32 v[6:7], v[6:7], v[8:9]
	v_add_f32_e32 v2, 1.0, v2
	v_rcp_f32_e32 v13, v2
	v_mov_b32_e32 v4, v3
	v_pk_mul_f32 v[6:7], v[14:15], v[6:7]
	v_pk_mul_f32 v[2:3], v[4:5], v[66:67] op_sel_hi:[1,0]
	v_pk_mul_f32 v[4:5], v[12:13], v[10:11]
	s_nop 0
	v_pk_mul_f32 v[2:3], v[2:3], v[4:5]
	v_and_b32_sdwa v4, v7, v177 dst_sel:DWORD dst_unused:UNUSED_PAD src0_sel:WORD_1 src1_sel:DWORD
	v_and_b32_sdwa v5, v6, v177 dst_sel:DWORD dst_unused:UNUSED_PAD src0_sel:WORD_1 src1_sel:DWORD
	v_add3_u32 v5, v6, v5, s63
	v_add3_u32 v4, v7, v4, s63
	v_and_b32_sdwa v6, v3, v177 dst_sel:DWORD dst_unused:UNUSED_PAD src0_sel:WORD_1 src1_sel:DWORD
	v_and_b32_sdwa v7, v2, v177 dst_sel:DWORD dst_unused:UNUSED_PAD src0_sel:WORD_1 src1_sel:DWORD
	v_add3_u32 v3, v3, v6, s63
	v_add3_u32 v2, v2, v7, s63
	v_and_b32_e32 v3, 0xffff0000, v3
	v_and_b32_e32 v2, 0xffff0000, v2
	v_or_b32_sdwa v3, v3, v4 dst_sel:DWORD dst_unused:UNUSED_PAD src0_sel:DWORD src1_sel:WORD_1
	v_or_b32_sdwa v2, v2, v5 dst_sel:DWORD dst_unused:UNUSED_PAD src0_sel:DWORD src1_sel:WORD_1
	global_store_dwordx2 v[74:75], v[2:3], off offset:480
	s_cbranch_scc1 .LBB0_389
